# hyena unit prologue: 12 boundary loads issued together with one wait; GEMM B-fragment LDS reads use immediate offsets (7 K-loops) instead of per-read address adds
# speedup vs baseline: 1.0247x; 1.0073x over previous
.LBB0_388:
	v_lshrrev_b32_e32 v20, 1, v10
	v_and_b32_e32 v20, 24, v20
	v_and_b32_e32 v11, 15, v10
	v_lshlrev_b32_e32 v21, 1, v20
	v_lshlrev_b32_e32 v10, 2, v10
	s_lshl_b32 s1, s1, 5
	v_lshl_or_b32 v1, s10, 6, v11
	s_lshl_b32 s10, s10, 13
	v_lshl_or_b32 v11, v11, 6, v21
	v_and_b32_e32 v10, 32, v10
	s_and_b32 s1, s1, 0x60
	v_lshl_add_u64 v[12:13], s[48:49], 0, v[2:3]
	v_mov_b32_e32 v133, v3
	v_readlane_b32 s46, v254, 40
	v_bitop3_b32 v21, v11, s10, v10 bitop3:0xde
	s_lshl_b32 s10, s1, 7
	v_lshl_add_u64 v[14:15], s[48:49], 0, v[132:133]
	v_mov_b32_e32 v137, v3
	v_readlane_b32 s47, v254, 41
	v_bitop3_b32 v142, v11, s10, v10 bitop3:0xde
	s_add_i32 m0, s56, 0x18000
	v_lshl_add_u64 v[10:11], v[12:13], 0, s[6:7]
	v_lshl_add_u64 v[16:17], s[46:47], 0, v[136:137]
	v_mov_b32_e32 v135, v3
	s_waitcnt vmcnt(2)
	s_barrier
	global_load_lds_dwordx4 v[10:11], off
	v_lshl_add_u64 v[10:11], v[14:15], 0, s[6:7]
	s_add_i32 m0, s56, 0x1a000
	s_add_i32 s60, s56, 0x8000
	s_add_i32 s61, s56, 0xa000
	v_lshl_add_u64 v[18:19], s[46:47], 0, v[134:135]
	global_load_lds_dwordx4 v[10:11], off
	v_lshl_add_u64 v[10:11], v[16:17], 0, s[6:7]
	s_mov_b32 m0, s60
	s_add_u32 s10, s48, 0x80080
	global_load_lds_dwordx4 v[10:11], off
	v_lshl_add_u64 v[10:11], v[18:19], 0, s[6:7]
	s_mov_b32 m0, s61
	s_addc_u32 s11, s49, 0
	global_load_lds_dwordx4 v[10:11], off
	s_add_i32 m0, s56, 0x1c000
	v_lshl_add_u64 v[10:11], s[10:11], 0, v[2:3]
	global_load_lds_dwordx4 v[10:11], off
	v_lshl_add_u64 v[10:11], s[10:11], 0, v[132:133]
	s_add_i32 m0, s56, 0x1e000
	s_cmpk_lt_u32 s0, 0x100
	global_load_lds_dwordx4 v[10:11], off
	v_lshlrev_b32_e32 v10, 15, v8
	v_and_b32_e32 v10, 0xffff0000, v10
	v_lshl_add_u32 v7, v7, 12, v10
	v_and_b32_e32 v8, 1, v8
	v_lshl_or_b32 v7, v8, 6, v7
	v_lshl_add_u32 v138, v9, 1, v7
	v_lshlrev_b32_e32 v7, 15, v4
	v_and_b32_e32 v7, 0xffff0000, v7
	s_waitcnt vmcnt(6)
	v_lshl_add_u32 v5, v5, 12, v7
	v_and_b32_e32 v4, 1, v4
	v_or_b32_e32 v144, s1, v20
	v_lshl_or_b32 v4, v4, 6, v5
	v_readlane_b32 s0, v254, 34
	v_or_b32_e32 v143, 0x400, v142
	v_add_u32_e32 v142, 0x10000, v142
	s_cselect_b64 s[36:37], -1, 0
	v_mov_b32_e32 v139, v3
	v_lshl_add_u32 v140, v6, 1, v4
	v_mov_b32_e32 v141, v3
	s_mov_b32 s62, 0
	v_add_u32_e32 v145, 0, v21
	v_readlane_b32 s63, v254, 33
	s_mov_b32 s64, s0
	s_barrier
	v_readlane_b32 s1, v254, 35
	s_waitcnt vmcnt(0)
	s_branch .LBB0_391

.LBB0_398:
	s_add_u32 s48, s46, 0xfff80080
	s_addc_u32 s49, s47, -1
	s_add_i32 s68, 0, 0x10000
	s_cmp_eq_u32 s67, 28
	s_cselect_b32 s53, s10, s49
	s_cselect_b32 s52, s11, s48
	s_cselect_b32 s49, s39, s66
	s_cselect_b32 s48, s41, s65
	s_add_i32 s70, 0, 0x14000
	ds_read_b128 v[146:149], v142
	ds_read_b128 v[150:153], v142 offset:1024
	ds_read_b128 v[154:157], v142 offset:2048
	ds_read_b128 v[158:161], v142 offset:3072
	ds_read_b128 v[162:165], v142 offset:16384
	ds_read_b128 v[166:169], v142 offset:17408
	ds_read_b128 v[170:173], v142 offset:18432
	ds_read_b128 v[178:181], v142 offset:19456
	v_lshl_add_u64 v[174:175], s[46:47], 0, v[138:139]
	s_add_i32 m0, s56, 0xc000
	ds_read_b128 v[182:185], v145
	ds_read_b128 v[186:189], v145 offset:1024
	ds_read_b128 v[190:193], v145 offset:2048
	ds_read_b128 v[194:197], v145 offset:3072
	ds_read_b128 v[198:201], v145 offset:4096
	ds_read_b128 v[202:205], v145 offset:5120
	ds_read_b128 v[206:209], v145 offset:6144
	ds_read_b128 v[226:229], v145 offset:7168
	global_load_lds_dwordx4 v[174:175], off
	v_lshl_add_u64 v[174:175], s[46:47], 0, v[140:141]
	s_add_i32 m0, s56, 0xe000
	s_nop 0
	global_load_lds_dwordx4 v[174:175], off
	s_waitcnt vmcnt(8)
	s_waitcnt lgkmcnt(0)
	s_barrier
	s_setprio 1
	s_waitcnt lgkmcnt(0)
	v_mfma_f32_16x16x32_bf16 v[128:131], v[146:149], v[182:185], v[128:131]
	v_mfma_f32_16x16x32_bf16 v[124:127], v[154:157], v[182:185], v[124:127]
	v_mfma_f32_16x16x32_bf16 v[120:123], v[146:149], v[190:193], v[120:123]
	v_mfma_f32_16x16x32_bf16 v[116:119], v[154:157], v[190:193], v[116:119]
	v_mfma_f32_16x16x32_bf16 v[104:107], v[146:149], v[198:201], v[104:107]
	v_mfma_f32_16x16x32_bf16 v[100:103], v[154:157], v[198:201], v[100:103]
	v_mfma_f32_16x16x32_bf16 v[88:91], v[146:149], v[206:209], v[88:91]
	v_mfma_f32_16x16x32_bf16 v[84:87], v[154:157], v[206:209], v[84:87]
	v_mfma_f32_16x16x32_bf16 v[128:131], v[150:153], v[186:189], v[128:131]
	v_mfma_f32_16x16x32_bf16 v[124:127], v[158:161], v[186:189], v[124:127]
	v_mfma_f32_16x16x32_bf16 v[120:123], v[150:153], v[194:197], v[120:123]
	v_mfma_f32_16x16x32_bf16 v[116:119], v[158:161], v[194:197], v[116:119]
	v_mfma_f32_16x16x32_bf16 v[104:107], v[150:153], v[202:205], v[104:107]
	v_mfma_f32_16x16x32_bf16 v[100:103], v[158:161], v[202:205], v[100:103]
	v_mfma_f32_16x16x32_bf16 v[88:91], v[150:153], v[226:229], v[88:91]
	v_mfma_f32_16x16x32_bf16 v[84:87], v[158:161], v[226:229], v[84:87]
	s_setprio 0
	s_setprio 1
	v_mfma_f32_16x16x32_bf16 v[112:115], v[162:165], v[182:185], v[112:115]
	v_mfma_f32_16x16x32_bf16 v[108:111], v[170:173], v[182:185], v[108:111]
	v_mfma_f32_16x16x32_bf16 v[96:99], v[162:165], v[190:193], v[96:99]
	v_mfma_f32_16x16x32_bf16 v[92:95], v[170:173], v[190:193], v[92:95]
	v_mfma_f32_16x16x32_bf16 v[80:83], v[162:165], v[198:201], v[80:83]
	v_mfma_f32_16x16x32_bf16 v[76:79], v[170:173], v[198:201], v[76:79]
	v_mfma_f32_16x16x32_bf16 v[72:75], v[162:165], v[206:209], v[72:75]
	v_mfma_f32_16x16x32_bf16 v[68:71], v[170:173], v[206:209], v[68:71]
	v_mfma_f32_16x16x32_bf16 v[112:115], v[166:169], v[186:189], v[112:115]
	v_mfma_f32_16x16x32_bf16 v[108:111], v[178:181], v[186:189], v[108:111]
	v_mfma_f32_16x16x32_bf16 v[96:99], v[166:169], v[194:197], v[96:99]
	v_mfma_f32_16x16x32_bf16 v[92:95], v[178:181], v[194:197], v[92:95]
	v_mfma_f32_16x16x32_bf16 v[80:83], v[166:169], v[202:205], v[80:83]
	v_mfma_f32_16x16x32_bf16 v[76:79], v[178:181], v[202:205], v[76:79]
	v_mfma_f32_16x16x32_bf16 v[72:75], v[166:169], v[226:229], v[72:75]
	v_mfma_f32_16x16x32_bf16 v[68:71], v[178:181], v[226:229], v[68:71]
	s_setprio 0
	s_barrier
	s_add_i32 s68, s68, s55
	v_lshl_add_u64 v[174:175], s[48:49], 0, v[2:3]
	s_mov_b32 m0, s68
	ds_read_b128 v[182:185], v145 offset:16384
	ds_read_b128 v[186:189], v145 offset:17408
	ds_read_b128 v[190:193], v145 offset:18432
	ds_read_b128 v[194:197], v145 offset:19456
	ds_read_b128 v[198:201], v145 offset:20480
	ds_read_b128 v[202:205], v145 offset:21504
	ds_read_b128 v[206:209], v145 offset:22528
	ds_read_b128 v[226:229], v145 offset:23552
	global_load_lds_dwordx4 v[174:175], off
	s_add_i32 m0, s68, 0x2000
	s_add_u32 s68, s48, 0x80000
	v_lshl_add_u64 v[210:211], s[48:49], 0, v[132:133]
	s_addc_u32 s69, s49, 0
	s_add_i32 s70, s70, s55
	global_load_lds_dwordx4 v[210:211], off
	v_lshl_add_u64 v[214:215], s[68:69], 0, v[2:3]
	s_mov_b32 m0, s70
	v_lshl_add_u64 v[230:231], s[52:53], 0, v[134:135]
	global_load_lds_dwordx4 v[214:215], off
	v_lshl_add_u64 v[214:215], s[68:69], 0, v[132:133]
	s_add_i32 m0, s70, 0x2000
	s_nop 0
	global_load_lds_dwordx4 v[214:215], off
	v_lshl_add_u64 v[214:215], s[52:53], 0, v[136:137]
	s_mov_b32 m0, s56
	s_nop 0
	global_load_lds_dwordx4 v[214:215], off
	s_mov_b32 m0, s57
	s_nop 0
	global_load_lds_dwordx4 v[230:231], off
	s_waitcnt vmcnt(8)
	s_waitcnt lgkmcnt(0)
	s_barrier
	s_setprio 1
	s_waitcnt lgkmcnt(0)
	v_mfma_f32_16x16x32_bf16 v[64:67], v[146:149], v[182:185], v[64:67]
	v_mfma_f32_16x16x32_bf16 v[60:63], v[154:157], v[182:185], v[60:63]
	v_mfma_f32_16x16x32_bf16 v[56:59], v[146:149], v[190:193], v[56:59]
	v_mfma_f32_16x16x32_bf16 v[52:55], v[154:157], v[190:193], v[52:55]
	v_mfma_f32_16x16x32_bf16 v[40:43], v[146:149], v[198:201], v[40:43]
	v_mfma_f32_16x16x32_bf16 v[36:39], v[154:157], v[198:201], v[36:39]
	v_mfma_f32_16x16x32_bf16 v[24:27], v[146:149], v[206:209], v[24:27]
	v_mfma_f32_16x16x32_bf16 v[20:23], v[154:157], v[206:209], v[20:23]
	v_mfma_f32_16x16x32_bf16 v[64:67], v[150:153], v[186:189], v[64:67]
	v_mfma_f32_16x16x32_bf16 v[60:63], v[158:161], v[186:189], v[60:63]
	v_mfma_f32_16x16x32_bf16 v[56:59], v[150:153], v[194:197], v[56:59]
	v_mfma_f32_16x16x32_bf16 v[52:55], v[158:161], v[194:197], v[52:55]
	v_mfma_f32_16x16x32_bf16 v[40:43], v[150:153], v[202:205], v[40:43]
	v_mfma_f32_16x16x32_bf16 v[36:39], v[158:161], v[202:205], v[36:39]
	v_mfma_f32_16x16x32_bf16 v[24:27], v[150:153], v[226:229], v[24:27]
	v_mfma_f32_16x16x32_bf16 v[20:23], v[158:161], v[226:229], v[20:23]
	s_setprio 0
	s_setprio 1
	v_mfma_f32_16x16x32_bf16 v[48:51], v[162:165], v[182:185], v[48:51]
	v_mfma_f32_16x16x32_bf16 v[44:47], v[170:173], v[182:185], v[44:47]
	v_mfma_f32_16x16x32_bf16 v[32:35], v[162:165], v[190:193], v[32:35]
	v_mfma_f32_16x16x32_bf16 v[28:31], v[170:173], v[190:193], v[28:31]
	v_mfma_f32_16x16x32_bf16 v[16:19], v[162:165], v[198:201], v[16:19]
	v_mfma_f32_16x16x32_bf16 v[12:15], v[170:173], v[198:201], v[12:15]
	v_mfma_f32_16x16x32_bf16 v[8:11], v[162:165], v[206:209], v[8:11]
	v_mfma_f32_16x16x32_bf16 v[4:7], v[170:173], v[206:209], v[4:7]
	v_mfma_f32_16x16x32_bf16 v[48:51], v[166:169], v[186:189], v[48:51]
	v_mfma_f32_16x16x32_bf16 v[44:47], v[178:181], v[186:189], v[44:47]
	v_mfma_f32_16x16x32_bf16 v[32:35], v[166:169], v[194:197], v[32:35]
	v_mfma_f32_16x16x32_bf16 v[28:31], v[178:181], v[194:197], v[28:31]
	v_mfma_f32_16x16x32_bf16 v[16:19], v[166:169], v[202:205], v[16:19]
	v_mfma_f32_16x16x32_bf16 v[12:15], v[178:181], v[202:205], v[12:15]
	v_mfma_f32_16x16x32_bf16 v[8:11], v[166:169], v[226:229], v[8:11]
	v_mfma_f32_16x16x32_bf16 v[4:7], v[178:181], v[226:229], v[4:7]
	s_setprio 0
	s_barrier
	s_add_i32 s68, 0, 0x18000
	s_add_i32 s69, 0, 0x1c000
	ds_read_b128 v[146:149], v142 offset:32768
	ds_read_b128 v[150:153], v142 offset:33792
	ds_read_b128 v[154:157], v142 offset:34816
	ds_read_b128 v[158:161], v142 offset:35840
	ds_read_b128 v[162:165], v142 offset:49152
	ds_read_b128 v[166:169], v142 offset:50176
	ds_read_b128 v[170:173], v142 offset:51200
	ds_read_b128 v[178:181], v142 offset:52224
	s_add_u32 s52, s52, 0x80000
	s_addc_u32 s53, s53, 0
	s_mov_b32 m0, s58
	v_lshl_add_u64 v[232:233], s[52:53], 0, v[136:137]
	ds_read_b128 v[182:185], v145 offset:32768
	ds_read_b128 v[186:189], v145 offset:33792
	ds_read_b128 v[190:193], v145 offset:34816
	ds_read_b128 v[194:197], v145 offset:35840
	ds_read_b128 v[198:201], v145 offset:36864
	ds_read_b128 v[202:205], v145 offset:37888
	ds_read_b128 v[206:209], v145 offset:38912
	ds_read_b128 v[226:229], v145 offset:39936
	global_load_lds_dwordx4 v[232:233], off
	v_lshl_add_u64 v[232:233], s[52:53], 0, v[134:135]
	s_mov_b32 m0, s59
	s_nop 0
	global_load_lds_dwordx4 v[232:233], off
	s_waitcnt vmcnt(8)
	s_waitcnt lgkmcnt(0)
	s_barrier
	s_setprio 1
	s_waitcnt lgkmcnt(0)
	v_mfma_f32_16x16x32_bf16 v[128:131], v[146:149], v[182:185], v[128:131]
	v_mfma_f32_16x16x32_bf16 v[124:127], v[154:157], v[182:185], v[124:127]
	v_mfma_f32_16x16x32_bf16 v[120:123], v[146:149], v[190:193], v[120:123]
	v_mfma_f32_16x16x32_bf16 v[116:119], v[154:157], v[190:193], v[116:119]
	v_mfma_f32_16x16x32_bf16 v[104:107], v[146:149], v[198:201], v[104:107]
	v_mfma_f32_16x16x32_bf16 v[100:103], v[154:157], v[198:201], v[100:103]
	v_mfma_f32_16x16x32_bf16 v[88:91], v[146:149], v[206:209], v[88:91]
	v_mfma_f32_16x16x32_bf16 v[84:87], v[154:157], v[206:209], v[84:87]
	v_mfma_f32_16x16x32_bf16 v[128:131], v[150:153], v[186:189], v[128:131]
	v_mfma_f32_16x16x32_bf16 v[124:127], v[158:161], v[186:189], v[124:127]
	v_mfma_f32_16x16x32_bf16 v[120:123], v[150:153], v[194:197], v[120:123]
	v_mfma_f32_16x16x32_bf16 v[116:119], v[158:161], v[194:197], v[116:119]
	v_mfma_f32_16x16x32_bf16 v[104:107], v[150:153], v[202:205], v[104:107]
	v_mfma_f32_16x16x32_bf16 v[100:103], v[158:161], v[202:205], v[100:103]
	v_mfma_f32_16x16x32_bf16 v[88:91], v[150:153], v[226:229], v[88:91]
	v_mfma_f32_16x16x32_bf16 v[84:87], v[158:161], v[226:229], v[84:87]
	s_setprio 0
	s_setprio 1
	v_mfma_f32_16x16x32_bf16 v[112:115], v[162:165], v[182:185], v[112:115]
	v_mfma_f32_16x16x32_bf16 v[108:111], v[170:173], v[182:185], v[108:111]
	v_mfma_f32_16x16x32_bf16 v[96:99], v[162:165], v[190:193], v[96:99]
	v_mfma_f32_16x16x32_bf16 v[92:95], v[170:173], v[190:193], v[92:95]
	v_mfma_f32_16x16x32_bf16 v[80:83], v[162:165], v[198:201], v[80:83]
	v_mfma_f32_16x16x32_bf16 v[76:79], v[170:173], v[198:201], v[76:79]
	v_mfma_f32_16x16x32_bf16 v[72:75], v[162:165], v[206:209], v[72:75]
	v_mfma_f32_16x16x32_bf16 v[68:71], v[170:173], v[206:209], v[68:71]
	v_mfma_f32_16x16x32_bf16 v[112:115], v[166:169], v[186:189], v[112:115]
	v_mfma_f32_16x16x32_bf16 v[108:111], v[178:181], v[186:189], v[108:111]
	v_mfma_f32_16x16x32_bf16 v[96:99], v[166:169], v[194:197], v[96:99]
	v_mfma_f32_16x16x32_bf16 v[92:95], v[178:181], v[194:197], v[92:95]
	v_mfma_f32_16x16x32_bf16 v[80:83], v[166:169], v[202:205], v[80:83]
	v_mfma_f32_16x16x32_bf16 v[76:79], v[178:181], v[202:205], v[76:79]
	v_mfma_f32_16x16x32_bf16 v[72:75], v[166:169], v[226:229], v[72:75]
	v_mfma_f32_16x16x32_bf16 v[68:71], v[178:181], v[226:229], v[68:71]
	s_setprio 0
	s_barrier
	s_add_i32 s52, s68, s55
	v_lshl_add_u64 v[174:175], v[174:175], 0, s[6:7]
	s_mov_b32 m0, s52
	ds_read_b128 v[182:185], v145 offset:49152
	ds_read_b128 v[186:189], v145 offset:50176
	ds_read_b128 v[190:193], v145 offset:51200
	ds_read_b128 v[194:197], v145 offset:52224
	ds_read_b128 v[198:201], v145 offset:53248
	ds_read_b128 v[202:205], v145 offset:54272
	ds_read_b128 v[206:209], v145 offset:55296
	ds_read_b128 v[226:229], v145 offset:56320
	global_load_lds_dwordx4 v[174:175], off
	s_add_i32 m0, s52, 0x2000
	s_add_u32 s48, s48, 0x80080
	v_lshl_add_u64 v[174:175], v[210:211], 0, s[6:7]
	s_addc_u32 s49, s49, 0
	s_add_i32 s52, s69, s55
	global_load_lds_dwordx4 v[174:175], off
	v_lshl_add_u64 v[174:175], s[48:49], 0, v[2:3]
	s_mov_b32 m0, s52
	s_nop 0
	global_load_lds_dwordx4 v[174:175], off
	v_lshl_add_u64 v[174:175], s[48:49], 0, v[132:133]
	s_add_i32 m0, s52, 0x2000
	s_nop 0
	global_load_lds_dwordx4 v[174:175], off
	v_lshl_add_u64 v[174:175], v[214:215], 0, s[6:7]
	s_mov_b32 m0, s60
	s_nop 0
	global_load_lds_dwordx4 v[174:175], off
	v_lshl_add_u64 v[174:175], v[230:231], 0, s[6:7]
	s_mov_b32 m0, s61
	s_nop 0
	global_load_lds_dwordx4 v[174:175], off
	s_waitcnt vmcnt(8)
	s_waitcnt lgkmcnt(0)
	s_barrier
	s_setprio 1
	s_waitcnt lgkmcnt(0)
	v_mfma_f32_16x16x32_bf16 v[64:67], v[146:149], v[182:185], v[64:67]
	v_mfma_f32_16x16x32_bf16 v[60:63], v[154:157], v[182:185], v[60:63]
	v_mfma_f32_16x16x32_bf16 v[56:59], v[146:149], v[190:193], v[56:59]
	v_mfma_f32_16x16x32_bf16 v[52:55], v[154:157], v[190:193], v[52:55]
	v_mfma_f32_16x16x32_bf16 v[40:43], v[146:149], v[198:201], v[40:43]
	v_mfma_f32_16x16x32_bf16 v[36:39], v[154:157], v[198:201], v[36:39]
	v_mfma_f32_16x16x32_bf16 v[24:27], v[146:149], v[206:209], v[24:27]
	v_mfma_f32_16x16x32_bf16 v[20:23], v[154:157], v[206:209], v[20:23]
	v_mfma_f32_16x16x32_bf16 v[64:67], v[150:153], v[186:189], v[64:67]
	v_mfma_f32_16x16x32_bf16 v[60:63], v[158:161], v[186:189], v[60:63]
	v_mfma_f32_16x16x32_bf16 v[56:59], v[150:153], v[194:197], v[56:59]
	v_mfma_f32_16x16x32_bf16 v[52:55], v[158:161], v[194:197], v[52:55]
	v_mfma_f32_16x16x32_bf16 v[40:43], v[150:153], v[202:205], v[40:43]
	v_mfma_f32_16x16x32_bf16 v[36:39], v[158:161], v[202:205], v[36:39]
	v_mfma_f32_16x16x32_bf16 v[24:27], v[150:153], v[226:229], v[24:27]
	v_mfma_f32_16x16x32_bf16 v[20:23], v[158:161], v[226:229], v[20:23]
	s_setprio 0
	s_setprio 1
	v_mfma_f32_16x16x32_bf16 v[48:51], v[162:165], v[182:185], v[48:51]
	v_mfma_f32_16x16x32_bf16 v[44:47], v[170:173], v[182:185], v[44:47]
	v_mfma_f32_16x16x32_bf16 v[32:35], v[162:165], v[190:193], v[32:35]
	v_mfma_f32_16x16x32_bf16 v[28:31], v[170:173], v[190:193], v[28:31]
	v_mfma_f32_16x16x32_bf16 v[16:19], v[162:165], v[198:201], v[16:19]
	v_mfma_f32_16x16x32_bf16 v[12:15], v[170:173], v[198:201], v[12:15]
	v_mfma_f32_16x16x32_bf16 v[8:11], v[162:165], v[206:209], v[8:11]
	v_mfma_f32_16x16x32_bf16 v[4:7], v[170:173], v[206:209], v[4:7]
	v_mfma_f32_16x16x32_bf16 v[48:51], v[166:169], v[186:189], v[48:51]
	v_mfma_f32_16x16x32_bf16 v[44:47], v[178:181], v[186:189], v[44:47]
	v_mfma_f32_16x16x32_bf16 v[32:35], v[166:169], v[194:197], v[32:35]
	v_mfma_f32_16x16x32_bf16 v[28:31], v[178:181], v[194:197], v[28:31]
	v_mfma_f32_16x16x32_bf16 v[16:19], v[166:169], v[202:205], v[16:19]
	v_mfma_f32_16x16x32_bf16 v[12:15], v[178:181], v[202:205], v[12:15]
	v_mfma_f32_16x16x32_bf16 v[8:11], v[166:169], v[226:229], v[8:11]
	v_mfma_f32_16x16x32_bf16 v[4:7], v[178:181], v[226:229], v[4:7]
	s_setprio 0
	s_barrier
	s_add_i32 s67, s67, 2
	s_add_u32 s46, s46, 0x100
	s_addc_u32 s47, s47, 0
	s_add_u32 s65, s65, 0x100
	s_addc_u32 s66, s66, 0
	s_cmp_gt_u32 s67, 29
	s_cbranch_scc0 .LBB0_398
	s_and_b64 vcc, exec, s[36:37]
	s_cbranch_vccz .LBB0_401
	s_barrier

.LBB0_575:
	v_lshrrev_b32_e32 v20, 1, v18
	v_and_b32_e32 v20, 24, v20
	v_and_b32_e32 v19, 15, v18
	v_lshlrev_b32_e32 v21, 1, v20
	v_lshlrev_b32_e32 v18, 2, v18
	s_lshl_b32 s1, s1, 5
	v_lshl_or_b32 v1, s10, 6, v19
	s_lshl_b32 s10, s10, 13
	v_lshl_or_b32 v19, v19, 6, v21
	v_and_b32_e32 v18, 32, v18
	s_and_b32 s1, s1, 0x60
	s_add_i32 m0, s39, 0x18000
	v_lshl_add_u64 v[10:11], v[10:11], 0, s[6:7]
	v_bitop3_b32 v21, v19, s10, v18 bitop3:0xde
	s_lshl_b32 s10, s1, 7
	s_waitcnt vmcnt(2)
	s_barrier
	global_load_lds_dwordx4 v[10:11], off
	v_lshl_add_u64 v[8:9], v[8:9], 0, s[6:7]
	s_add_i32 m0, s39, 0x1a000
	s_add_i32 s70, s39, 0x8000
	s_add_i32 s71, s39, 0xa000
	v_bitop3_b32 v142, v19, s10, v18 bitop3:0xde
	global_load_lds_dwordx4 v[8:9], off
	v_lshl_add_u64 v[4:5], v[4:5], 0, s[6:7]
	s_mov_b32 m0, s70
	s_add_u32 s10, s58, 0x20080
	global_load_lds_dwordx4 v[4:5], off
	v_lshl_add_u64 v[4:5], v[6:7], 0, s[6:7]
	s_mov_b32 m0, s71
	s_addc_u32 s11, s59, 0
	global_load_lds_dwordx4 v[4:5], off
	s_add_i32 m0, s39, 0x1c000
	v_lshl_add_u64 v[4:5], s[10:11], 0, v[2:3]
	global_load_lds_dwordx4 v[4:5], off
	v_lshl_add_u64 v[4:5], s[10:11], 0, v[132:133]
	s_add_i32 m0, s39, 0x1e000
	s_cmpk_lt_u32 s0, 0x100
	global_load_lds_dwordx4 v[4:5], off
	v_lshlrev_b32_e32 v4, 13, v16
	v_and_b32_e32 v4, 0xffffc000, v4
	v_lshl_add_u32 v4, v15, 10, v4
	v_and_b32_e32 v5, 1, v16
	v_lshl_or_b32 v4, v5, 6, v4
	v_lshl_add_u32 v138, v17, 1, v4
	v_lshlrev_b32_e32 v4, 13, v12
	v_and_b32_e32 v4, 0xffffc000, v4
	s_waitcnt vmcnt(6)
	v_lshl_add_u32 v4, v13, 10, v4
	v_and_b32_e32 v5, 1, v12
	v_lshl_or_b32 v4, v5, 6, v4
	v_or_b32_e32 v143, 0x400, v142
	v_add_u32_e32 v142, 0x10000, v142
	s_cselect_b64 s[44:45], -1, 0
	v_or_b32_e32 v144, s1, v20
	v_mov_b32_e32 v139, v3
	v_lshl_add_u32 v140, v14, 1, v4
	v_mov_b32_e32 v141, v3
	s_mov_b32 s72, 0
	v_add_u32_e32 v145, 0, v21
	s_barrier
	s_branch .LBB0_578

.LBB0_585:
	s_add_u32 s42, s56, 0xfffe0080
	s_addc_u32 s43, s57, -1
	s_add_i32 s76, 0, 0x10000
	s_cmp_eq_u32 s75, 4
	s_cselect_b32 s61, s10, s43
	s_cselect_b32 s60, s11, s42
	s_cselect_b32 s59, s47, s74
	s_cselect_b32 s58, s49, s73
	s_add_i32 s77, 0, 0x14000
	ds_read_b128 v[146:149], v142
	ds_read_b128 v[150:153], v142 offset:1024
	ds_read_b128 v[154:157], v142 offset:2048
	ds_read_b128 v[158:161], v142 offset:3072
	ds_read_b128 v[162:165], v142 offset:16384
	ds_read_b128 v[166:169], v142 offset:17408
	ds_read_b128 v[170:173], v142 offset:18432
	ds_read_b128 v[178:181], v142 offset:19456
	v_lshl_add_u64 v[174:175], s[56:57], 0, v[138:139]
	s_add_i32 m0, s39, 0xc000
	ds_read_b128 v[182:185], v145
	ds_read_b128 v[186:189], v145 offset:1024
	ds_read_b128 v[190:193], v145 offset:2048
	ds_read_b128 v[194:197], v145 offset:3072
	ds_read_b128 v[198:201], v145 offset:4096
	ds_read_b128 v[202:205], v145 offset:5120
	ds_read_b128 v[206:209], v145 offset:6144
	ds_read_b128 v[226:229], v145 offset:7168
	global_load_lds_dwordx4 v[174:175], off
	v_lshl_add_u64 v[174:175], s[56:57], 0, v[140:141]
	s_add_i32 m0, s39, 0xe000
	s_nop 0
	global_load_lds_dwordx4 v[174:175], off
	s_waitcnt vmcnt(8)
	s_waitcnt lgkmcnt(0)
	s_barrier
	s_setprio 1
	s_waitcnt lgkmcnt(0)
	v_mfma_f32_16x16x32_bf16 v[128:131], v[146:149], v[182:185], v[128:131]
	v_mfma_f32_16x16x32_bf16 v[124:127], v[154:157], v[182:185], v[124:127]
	v_mfma_f32_16x16x32_bf16 v[120:123], v[146:149], v[190:193], v[120:123]
	v_mfma_f32_16x16x32_bf16 v[116:119], v[154:157], v[190:193], v[116:119]
	v_mfma_f32_16x16x32_bf16 v[104:107], v[146:149], v[198:201], v[104:107]
	v_mfma_f32_16x16x32_bf16 v[100:103], v[154:157], v[198:201], v[100:103]
	v_mfma_f32_16x16x32_bf16 v[88:91], v[146:149], v[206:209], v[88:91]
	v_mfma_f32_16x16x32_bf16 v[84:87], v[154:157], v[206:209], v[84:87]
	v_mfma_f32_16x16x32_bf16 v[128:131], v[150:153], v[186:189], v[128:131]
	v_mfma_f32_16x16x32_bf16 v[124:127], v[158:161], v[186:189], v[124:127]
	v_mfma_f32_16x16x32_bf16 v[120:123], v[150:153], v[194:197], v[120:123]
	v_mfma_f32_16x16x32_bf16 v[116:119], v[158:161], v[194:197], v[116:119]
	v_mfma_f32_16x16x32_bf16 v[104:107], v[150:153], v[202:205], v[104:107]
	v_mfma_f32_16x16x32_bf16 v[100:103], v[158:161], v[202:205], v[100:103]
	v_mfma_f32_16x16x32_bf16 v[88:91], v[150:153], v[226:229], v[88:91]
	v_mfma_f32_16x16x32_bf16 v[84:87], v[158:161], v[226:229], v[84:87]
	s_setprio 0
	s_setprio 1
	v_mfma_f32_16x16x32_bf16 v[112:115], v[162:165], v[182:185], v[112:115]
	v_mfma_f32_16x16x32_bf16 v[108:111], v[170:173], v[182:185], v[108:111]
	v_mfma_f32_16x16x32_bf16 v[96:99], v[162:165], v[190:193], v[96:99]
	v_mfma_f32_16x16x32_bf16 v[92:95], v[170:173], v[190:193], v[92:95]
	v_mfma_f32_16x16x32_bf16 v[80:83], v[162:165], v[198:201], v[80:83]
	v_mfma_f32_16x16x32_bf16 v[76:79], v[170:173], v[198:201], v[76:79]
	v_mfma_f32_16x16x32_bf16 v[72:75], v[162:165], v[206:209], v[72:75]
	v_mfma_f32_16x16x32_bf16 v[68:71], v[170:173], v[206:209], v[68:71]
	v_mfma_f32_16x16x32_bf16 v[112:115], v[166:169], v[186:189], v[112:115]
	v_mfma_f32_16x16x32_bf16 v[108:111], v[178:181], v[186:189], v[108:111]
	v_mfma_f32_16x16x32_bf16 v[96:99], v[166:169], v[194:197], v[96:99]
	v_mfma_f32_16x16x32_bf16 v[92:95], v[178:181], v[194:197], v[92:95]
	v_mfma_f32_16x16x32_bf16 v[80:83], v[166:169], v[202:205], v[80:83]
	v_mfma_f32_16x16x32_bf16 v[76:79], v[178:181], v[202:205], v[76:79]
	v_mfma_f32_16x16x32_bf16 v[72:75], v[166:169], v[226:229], v[72:75]
	v_mfma_f32_16x16x32_bf16 v[68:71], v[178:181], v[226:229], v[68:71]
	s_setprio 0
	s_barrier
	s_add_i32 s42, s76, s67
	v_lshl_add_u64 v[174:175], s[58:59], 0, v[2:3]
	s_mov_b32 m0, s42
	ds_read_b128 v[182:185], v145 offset:16384
	ds_read_b128 v[186:189], v145 offset:17408
	ds_read_b128 v[190:193], v145 offset:18432
	ds_read_b128 v[194:197], v145 offset:19456
	ds_read_b128 v[198:201], v145 offset:20480
	ds_read_b128 v[202:205], v145 offset:21504
	ds_read_b128 v[206:209], v145 offset:22528
	ds_read_b128 v[226:229], v145 offset:23552
	global_load_lds_dwordx4 v[174:175], off
	s_add_i32 m0, s42, 0x2000
	s_add_u32 s42, s58, 0x20000
	v_lshl_add_u64 v[210:211], s[58:59], 0, v[132:133]
	s_addc_u32 s43, s59, 0
	s_add_i32 s76, s77, s67
	global_load_lds_dwordx4 v[210:211], off
	v_lshl_add_u64 v[214:215], s[42:43], 0, v[2:3]
	s_mov_b32 m0, s76
	v_lshl_add_u64 v[230:231], s[60:61], 0, v[134:135]
	global_load_lds_dwordx4 v[214:215], off
	v_lshl_add_u64 v[214:215], s[42:43], 0, v[132:133]
	s_add_i32 m0, s76, 0x2000
	s_nop 0
	global_load_lds_dwordx4 v[214:215], off
	v_lshl_add_u64 v[214:215], s[60:61], 0, v[136:137]
	s_mov_b32 m0, s39
	s_nop 0
	global_load_lds_dwordx4 v[214:215], off
	s_mov_b32 m0, s41
	s_nop 0
	global_load_lds_dwordx4 v[230:231], off
	s_waitcnt vmcnt(8)
	s_waitcnt lgkmcnt(0)
	s_barrier
	s_setprio 1
	s_waitcnt lgkmcnt(0)
	v_mfma_f32_16x16x32_bf16 v[64:67], v[146:149], v[182:185], v[64:67]
	v_mfma_f32_16x16x32_bf16 v[60:63], v[154:157], v[182:185], v[60:63]
	v_mfma_f32_16x16x32_bf16 v[56:59], v[146:149], v[190:193], v[56:59]
	v_mfma_f32_16x16x32_bf16 v[52:55], v[154:157], v[190:193], v[52:55]
	v_mfma_f32_16x16x32_bf16 v[40:43], v[146:149], v[198:201], v[40:43]
	v_mfma_f32_16x16x32_bf16 v[36:39], v[154:157], v[198:201], v[36:39]
	v_mfma_f32_16x16x32_bf16 v[24:27], v[146:149], v[206:209], v[24:27]
	v_mfma_f32_16x16x32_bf16 v[20:23], v[154:157], v[206:209], v[20:23]
	v_mfma_f32_16x16x32_bf16 v[64:67], v[150:153], v[186:189], v[64:67]
	v_mfma_f32_16x16x32_bf16 v[60:63], v[158:161], v[186:189], v[60:63]
	v_mfma_f32_16x16x32_bf16 v[56:59], v[150:153], v[194:197], v[56:59]
	v_mfma_f32_16x16x32_bf16 v[52:55], v[158:161], v[194:197], v[52:55]
	v_mfma_f32_16x16x32_bf16 v[40:43], v[150:153], v[202:205], v[40:43]
	v_mfma_f32_16x16x32_bf16 v[36:39], v[158:161], v[202:205], v[36:39]
	v_mfma_f32_16x16x32_bf16 v[24:27], v[150:153], v[226:229], v[24:27]
	v_mfma_f32_16x16x32_bf16 v[20:23], v[158:161], v[226:229], v[20:23]
	s_setprio 0
	s_setprio 1
	v_mfma_f32_16x16x32_bf16 v[48:51], v[162:165], v[182:185], v[48:51]
	v_mfma_f32_16x16x32_bf16 v[44:47], v[170:173], v[182:185], v[44:47]
	v_mfma_f32_16x16x32_bf16 v[32:35], v[162:165], v[190:193], v[32:35]
	v_mfma_f32_16x16x32_bf16 v[28:31], v[170:173], v[190:193], v[28:31]
	v_mfma_f32_16x16x32_bf16 v[16:19], v[162:165], v[198:201], v[16:19]
	v_mfma_f32_16x16x32_bf16 v[12:15], v[170:173], v[198:201], v[12:15]
	v_mfma_f32_16x16x32_bf16 v[8:11], v[162:165], v[206:209], v[8:11]
	v_mfma_f32_16x16x32_bf16 v[4:7], v[170:173], v[206:209], v[4:7]
	v_mfma_f32_16x16x32_bf16 v[48:51], v[166:169], v[186:189], v[48:51]
	v_mfma_f32_16x16x32_bf16 v[44:47], v[178:181], v[186:189], v[44:47]
	v_mfma_f32_16x16x32_bf16 v[32:35], v[166:169], v[194:197], v[32:35]
	v_mfma_f32_16x16x32_bf16 v[28:31], v[178:181], v[194:197], v[28:31]
	v_mfma_f32_16x16x32_bf16 v[16:19], v[166:169], v[202:205], v[16:19]
	v_mfma_f32_16x16x32_bf16 v[12:15], v[178:181], v[202:205], v[12:15]
	v_mfma_f32_16x16x32_bf16 v[8:11], v[166:169], v[226:229], v[8:11]
	v_mfma_f32_16x16x32_bf16 v[4:7], v[178:181], v[226:229], v[4:7]
	s_setprio 0
	s_barrier
	s_add_i32 s76, 0, 0x18000
	s_add_i32 s77, 0, 0x1c000
	ds_read_b128 v[146:149], v142 offset:32768
	ds_read_b128 v[150:153], v142 offset:33792
	ds_read_b128 v[154:157], v142 offset:34816
	ds_read_b128 v[158:161], v142 offset:35840
	ds_read_b128 v[162:165], v142 offset:49152
	ds_read_b128 v[166:169], v142 offset:50176
	ds_read_b128 v[170:173], v142 offset:51200
	ds_read_b128 v[178:181], v142 offset:52224
	s_add_u32 s42, s60, 0x20000
	s_addc_u32 s43, s61, 0
	s_mov_b32 m0, s68
	v_lshl_add_u64 v[232:233], s[42:43], 0, v[136:137]
	ds_read_b128 v[182:185], v145 offset:32768
	ds_read_b128 v[186:189], v145 offset:33792
	ds_read_b128 v[190:193], v145 offset:34816
	ds_read_b128 v[194:197], v145 offset:35840
	ds_read_b128 v[198:201], v145 offset:36864
	ds_read_b128 v[202:205], v145 offset:37888
	ds_read_b128 v[206:209], v145 offset:38912
	ds_read_b128 v[226:229], v145 offset:39936
	global_load_lds_dwordx4 v[232:233], off
	v_lshl_add_u64 v[232:233], s[42:43], 0, v[134:135]
	s_mov_b32 m0, s69
	s_nop 0
	global_load_lds_dwordx4 v[232:233], off
	s_waitcnt vmcnt(8)
	s_waitcnt lgkmcnt(0)
	s_barrier
	s_setprio 1
	s_waitcnt lgkmcnt(0)
	v_mfma_f32_16x16x32_bf16 v[128:131], v[146:149], v[182:185], v[128:131]
	v_mfma_f32_16x16x32_bf16 v[124:127], v[154:157], v[182:185], v[124:127]
	v_mfma_f32_16x16x32_bf16 v[120:123], v[146:149], v[190:193], v[120:123]
	v_mfma_f32_16x16x32_bf16 v[116:119], v[154:157], v[190:193], v[116:119]
	v_mfma_f32_16x16x32_bf16 v[104:107], v[146:149], v[198:201], v[104:107]
	v_mfma_f32_16x16x32_bf16 v[100:103], v[154:157], v[198:201], v[100:103]
	v_mfma_f32_16x16x32_bf16 v[88:91], v[146:149], v[206:209], v[88:91]
	v_mfma_f32_16x16x32_bf16 v[84:87], v[154:157], v[206:209], v[84:87]
	v_mfma_f32_16x16x32_bf16 v[128:131], v[150:153], v[186:189], v[128:131]
	v_mfma_f32_16x16x32_bf16 v[124:127], v[158:161], v[186:189], v[124:127]
	v_mfma_f32_16x16x32_bf16 v[120:123], v[150:153], v[194:197], v[120:123]
	v_mfma_f32_16x16x32_bf16 v[116:119], v[158:161], v[194:197], v[116:119]
	v_mfma_f32_16x16x32_bf16 v[104:107], v[150:153], v[202:205], v[104:107]
	v_mfma_f32_16x16x32_bf16 v[100:103], v[158:161], v[202:205], v[100:103]
	v_mfma_f32_16x16x32_bf16 v[88:91], v[150:153], v[226:229], v[88:91]
	v_mfma_f32_16x16x32_bf16 v[84:87], v[158:161], v[226:229], v[84:87]
	s_setprio 0
	s_setprio 1
	v_mfma_f32_16x16x32_bf16 v[112:115], v[162:165], v[182:185], v[112:115]
	v_mfma_f32_16x16x32_bf16 v[108:111], v[170:173], v[182:185], v[108:111]
	v_mfma_f32_16x16x32_bf16 v[96:99], v[162:165], v[190:193], v[96:99]
	v_mfma_f32_16x16x32_bf16 v[92:95], v[170:173], v[190:193], v[92:95]
	v_mfma_f32_16x16x32_bf16 v[80:83], v[162:165], v[198:201], v[80:83]
	v_mfma_f32_16x16x32_bf16 v[76:79], v[170:173], v[198:201], v[76:79]
	v_mfma_f32_16x16x32_bf16 v[72:75], v[162:165], v[206:209], v[72:75]
	v_mfma_f32_16x16x32_bf16 v[68:71], v[170:173], v[206:209], v[68:71]
	v_mfma_f32_16x16x32_bf16 v[112:115], v[166:169], v[186:189], v[112:115]
	v_mfma_f32_16x16x32_bf16 v[108:111], v[178:181], v[186:189], v[108:111]
	v_mfma_f32_16x16x32_bf16 v[96:99], v[166:169], v[194:197], v[96:99]
	v_mfma_f32_16x16x32_bf16 v[92:95], v[178:181], v[194:197], v[92:95]
	v_mfma_f32_16x16x32_bf16 v[80:83], v[166:169], v[202:205], v[80:83]
	v_mfma_f32_16x16x32_bf16 v[76:79], v[178:181], v[202:205], v[76:79]
	v_mfma_f32_16x16x32_bf16 v[72:75], v[166:169], v[226:229], v[72:75]
	v_mfma_f32_16x16x32_bf16 v[68:71], v[178:181], v[226:229], v[68:71]
	s_setprio 0
	s_barrier
	s_add_i32 s42, s76, s67
	v_lshl_add_u64 v[174:175], v[174:175], 0, s[6:7]
	s_mov_b32 m0, s42
	ds_read_b128 v[182:185], v145 offset:49152
	ds_read_b128 v[186:189], v145 offset:50176
	ds_read_b128 v[190:193], v145 offset:51200
	ds_read_b128 v[194:197], v145 offset:52224
	ds_read_b128 v[198:201], v145 offset:53248
	ds_read_b128 v[202:205], v145 offset:54272
	ds_read_b128 v[206:209], v145 offset:55296
	ds_read_b128 v[226:229], v145 offset:56320
	global_load_lds_dwordx4 v[174:175], off
	s_add_i32 m0, s42, 0x2000
	s_add_u32 s42, s58, 0x20080
	v_lshl_add_u64 v[174:175], v[210:211], 0, s[6:7]
	s_addc_u32 s43, s59, 0
	s_add_i32 s58, s77, s67
	global_load_lds_dwordx4 v[174:175], off
	v_lshl_add_u64 v[174:175], s[42:43], 0, v[2:3]
	s_mov_b32 m0, s58
	s_nop 0
	global_load_lds_dwordx4 v[174:175], off
	v_lshl_add_u64 v[174:175], s[42:43], 0, v[132:133]
	s_add_i32 m0, s58, 0x2000
	s_nop 0
	global_load_lds_dwordx4 v[174:175], off
	v_lshl_add_u64 v[174:175], v[214:215], 0, s[6:7]
	s_mov_b32 m0, s70
	s_nop 0
	global_load_lds_dwordx4 v[174:175], off
	v_lshl_add_u64 v[174:175], v[230:231], 0, s[6:7]
	s_mov_b32 m0, s71
	s_nop 0
	global_load_lds_dwordx4 v[174:175], off
	s_waitcnt vmcnt(8)
	s_waitcnt lgkmcnt(0)
	s_barrier
	s_setprio 1
	s_waitcnt lgkmcnt(0)
	v_mfma_f32_16x16x32_bf16 v[64:67], v[146:149], v[182:185], v[64:67]
	v_mfma_f32_16x16x32_bf16 v[60:63], v[154:157], v[182:185], v[60:63]
	v_mfma_f32_16x16x32_bf16 v[56:59], v[146:149], v[190:193], v[56:59]
	v_mfma_f32_16x16x32_bf16 v[52:55], v[154:157], v[190:193], v[52:55]
	v_mfma_f32_16x16x32_bf16 v[40:43], v[146:149], v[198:201], v[40:43]
	v_mfma_f32_16x16x32_bf16 v[36:39], v[154:157], v[198:201], v[36:39]
	v_mfma_f32_16x16x32_bf16 v[24:27], v[146:149], v[206:209], v[24:27]
	v_mfma_f32_16x16x32_bf16 v[20:23], v[154:157], v[206:209], v[20:23]
	v_mfma_f32_16x16x32_bf16 v[64:67], v[150:153], v[186:189], v[64:67]
	v_mfma_f32_16x16x32_bf16 v[60:63], v[158:161], v[186:189], v[60:63]
	v_mfma_f32_16x16x32_bf16 v[56:59], v[150:153], v[194:197], v[56:59]
	v_mfma_f32_16x16x32_bf16 v[52:55], v[158:161], v[194:197], v[52:55]
	v_mfma_f32_16x16x32_bf16 v[40:43], v[150:153], v[202:205], v[40:43]
	v_mfma_f32_16x16x32_bf16 v[36:39], v[158:161], v[202:205], v[36:39]
	v_mfma_f32_16x16x32_bf16 v[24:27], v[150:153], v[226:229], v[24:27]
	v_mfma_f32_16x16x32_bf16 v[20:23], v[158:161], v[226:229], v[20:23]
	s_setprio 0
	s_setprio 1
	v_mfma_f32_16x16x32_bf16 v[48:51], v[162:165], v[182:185], v[48:51]
	v_mfma_f32_16x16x32_bf16 v[44:47], v[170:173], v[182:185], v[44:47]
	v_mfma_f32_16x16x32_bf16 v[32:35], v[162:165], v[190:193], v[32:35]
	v_mfma_f32_16x16x32_bf16 v[28:31], v[170:173], v[190:193], v[28:31]
	v_mfma_f32_16x16x32_bf16 v[16:19], v[162:165], v[198:201], v[16:19]
	v_mfma_f32_16x16x32_bf16 v[12:15], v[170:173], v[198:201], v[12:15]
	v_mfma_f32_16x16x32_bf16 v[8:11], v[162:165], v[206:209], v[8:11]
	v_mfma_f32_16x16x32_bf16 v[4:7], v[170:173], v[206:209], v[4:7]
	v_mfma_f32_16x16x32_bf16 v[48:51], v[166:169], v[186:189], v[48:51]
	v_mfma_f32_16x16x32_bf16 v[44:47], v[178:181], v[186:189], v[44:47]
	v_mfma_f32_16x16x32_bf16 v[32:35], v[166:169], v[194:197], v[32:35]
	v_mfma_f32_16x16x32_bf16 v[28:31], v[178:181], v[194:197], v[28:31]
	v_mfma_f32_16x16x32_bf16 v[16:19], v[166:169], v[202:205], v[16:19]
	v_mfma_f32_16x16x32_bf16 v[12:15], v[178:181], v[202:205], v[12:15]
	v_mfma_f32_16x16x32_bf16 v[8:11], v[166:169], v[226:229], v[8:11]
	v_mfma_f32_16x16x32_bf16 v[4:7], v[178:181], v[226:229], v[4:7]
	s_setprio 0
	s_barrier
	s_add_i32 s75, s75, 2
	s_add_u32 s56, s56, 0x100
	s_addc_u32 s57, s57, 0
	s_add_u32 s73, s73, 0x100
	s_addc_u32 s74, s74, 0
	s_cmp_gt_u32 s75, 5
	s_cbranch_scc0 .LBB0_585
	s_and_b64 vcc, exec, s[44:45]
	s_cbranch_vccz .LBB0_588
	s_barrier

.LBB0_643:
	v_mov_b32_e32 v1, v0
	s_movk_i32 s0, 0x50
	s_nop 0
	v_readfirstlane_b32 s48, v1
	v_cmp_gt_i32_e32 vcc, s0, v1
	s_and_saveexec_b64 s[0:1], vcc
	v_lshl_add_u32 v2, v1, 1, 0
	v_add_u32_e32 v2, 0x1a100, v2
	ds_write_b16 v2, v3
	s_or_b64 exec, exec, s[0:1]
	s_ashr_i32 s47, s46, 31
	s_lshl_b64 s[44:45], s[46:47], 14
	v_lshlrev_b32_e32 v28, 3, v1
	s_add_u32 s0, s58, s44
	v_add_u32_e32 v30, 0x1000, v28
	s_addc_u32 s1, s59, s45
	v_ashrrev_i32_e32 v31, 31, v30
	v_ashrrev_i32_e32 v2, 1, v1
	v_readlane_b32 s20, v251, 22
	v_lshl_add_u64 v[4:5], v[30:31], 1, s[0:1]
	s_add_i32 s38, s46, 0x80
	v_and_b32_e32 v2, 0xfffffe00, v2
	v_readlane_b32 s21, v251, 23
	v_ashrrev_i32_e32 v29, 31, v28
	global_load_dwordx4 v[82:85], v[4:5], off
	v_add_u32_e32 v2, s38, v2
	v_mov_b64_e32 v[4:5], s[20:21]
	s_movk_i32 s22, 0x4400
	v_lshl_add_u64 v[8:9], v[28:29], 1, s[0:1]
	v_mad_i64_i32 v[4:5], s[0:1], v2, s22, v[4:5]
	v_and_b32_e32 v2, 0x1000, v28
	v_and_b32_e32 v59, 0xff8, v28
	v_lshlrev_b32_e32 v2, 1, v2
	v_lshl_add_u64 v[6:7], v[4:5], 0, v[2:3]
	v_lshlrev_b32_e32 v4, 1, v59
	v_mov_b32_e32 v5, v3
	v_lshl_add_u64 v[6:7], v[6:7], 0, v[4:5]
	global_load_dwordx4 v[86:89], v[8:9], off
	global_load_dwordx4 v[24:27], v[6:7], off
	v_cmp_ne_u32_e32 vcc, 0, v59
	v_mov_b32_e32 v53, 0
	v_mov_b32_e32 v54, 0
	s_and_saveexec_b64 s[0:1], vcc
	s_movk_i32 s23, 0x3ff
	s_movk_i32 s24, 0x2800
	s_cbranch_execz .LBB0_647
	global_load_ushort v54, v[6:7], off offset:-2
.LBB0_647:
	s_or_b64 exec, exec, s[0:1]
	s_movk_i32 s0, 0xff8
	v_cmp_ne_u32_e64 s[0:1], s0, v59
	s_and_saveexec_b64 s[10:11], s[0:1]
	s_cbranch_execz .LBB0_649
	global_load_ushort v53, v[6:7], off offset:16
.LBB0_649:
	s_or_b64 exec, exec, s[10:11]
	v_add_u32_e32 v58, 0x200, v1
	v_ashrrev_i32_e32 v5, 1, v58
	v_and_b32_e32 v5, 0xfffffe00, v5
	v_add_u32_e32 v5, s38, v5
	v_mov_b64_e32 v[6:7], s[20:21]
	v_mad_i64_i32 v[6:7], s[10:11], v5, s22, v[6:7]
	v_lshlrev_b32_e32 v5, 4, v58
	v_and_b32_e32 v8, 0x2000, v5
	v_mov_b32_e32 v9, v3
	v_lshl_add_u64 v[6:7], v[6:7], 0, v[8:9]
	v_mov_b32_e32 v5, v3
	v_lshl_add_u64 v[6:7], v[6:7], 0, v[4:5]
	global_load_dwordx4 v[20:23], v[6:7], off
	v_mov_b32_e32 v49, 0
	v_mov_b32_e32 v50, 0
	s_and_saveexec_b64 s[10:11], vcc
	s_cbranch_execz .LBB0_651
	global_load_ushort v50, v[6:7], off offset:-2
.LBB0_651:
	s_or_b64 exec, exec, s[10:11]
	s_and_saveexec_b64 s[10:11], s[0:1]
	s_cbranch_execz .LBB0_653
	global_load_ushort v49, v[6:7], off offset:16
.LBB0_653:
	s_or_b64 exec, exec, s[10:11]
	v_add_u32_e32 v60, 0x400, v1
	v_ashrrev_i32_e32 v5, 1, v60
	v_and_b32_e32 v5, 0xfffffe00, v5
	v_add_u32_e32 v5, s38, v5
	v_mov_b64_e32 v[6:7], s[20:21]
	v_mad_i64_i32 v[6:7], s[10:11], v5, s22, v[6:7]
	v_lshl_add_u64 v[6:7], v[6:7], 0, v[2:3]
	v_mov_b32_e32 v5, v3
	v_lshl_add_u64 v[6:7], v[6:7], 0, v[4:5]
	global_load_dwordx4 v[16:19], v[6:7], off
	v_mov_b32_e32 v45, 0
	v_mov_b32_e32 v46, 0
	s_and_saveexec_b64 s[10:11], vcc
	s_cbranch_execz .LBB0_655
	global_load_ushort v46, v[6:7], off offset:-2
.LBB0_655:
	s_or_b64 exec, exec, s[10:11]
	s_and_saveexec_b64 s[10:11], s[0:1]
	s_cbranch_execz .LBB0_657
	global_load_ushort v45, v[6:7], off offset:16
.LBB0_657:
	s_or_b64 exec, exec, s[10:11]
	v_add_u32_e32 v61, 0x600, v1
	v_ashrrev_i32_e32 v5, 1, v61
	v_and_b32_e32 v5, 0xfffffe00, v5
	v_add_u32_e32 v5, s38, v5
	v_mov_b64_e32 v[6:7], s[20:21]
	v_mad_i64_i32 v[6:7], s[10:11], v5, s22, v[6:7]
	v_lshlrev_b32_e32 v5, 4, v61
	v_and_b32_e32 v8, 0x2000, v5
	v_mov_b32_e32 v9, v3
	v_lshl_add_u64 v[6:7], v[6:7], 0, v[8:9]
	v_mov_b32_e32 v5, v3
	v_lshl_add_u64 v[6:7], v[6:7], 0, v[4:5]
	global_load_dwordx4 v[12:15], v[6:7], off
	v_mov_b32_e32 v41, 0
	v_mov_b32_e32 v42, 0
	s_and_saveexec_b64 s[10:11], vcc
	s_cbranch_execz .LBB0_659
	global_load_ushort v42, v[6:7], off offset:-2
.LBB0_659:
	s_or_b64 exec, exec, s[10:11]
	s_and_saveexec_b64 s[10:11], s[0:1]
	s_cbranch_execz .LBB0_661
	global_load_ushort v41, v[6:7], off offset:16
.LBB0_661:
	s_or_b64 exec, exec, s[10:11]
	v_add_u32_e32 v39, 0x800, v1
	v_ashrrev_i32_e32 v5, 1, v39
	v_and_b32_e32 v5, 0xfffffe00, v5
	v_add_u32_e32 v5, s38, v5
	v_mov_b64_e32 v[6:7], s[20:21]
	v_mad_i64_i32 v[6:7], s[10:11], v5, s22, v[6:7]
	v_lshl_add_u64 v[6:7], v[6:7], 0, v[2:3]
	v_mov_b32_e32 v5, v3
	v_lshl_add_u64 v[6:7], v[6:7], 0, v[4:5]
	global_load_dwordx4 v[8:11], v[6:7], off
	v_mov_b32_e32 v37, 0
	v_mov_b32_e32 v38, 0
	s_and_saveexec_b64 s[10:11], vcc
	s_cbranch_execz .LBB0_663
	global_load_ushort v38, v[6:7], off offset:-2
.LBB0_663:
	s_or_b64 exec, exec, s[10:11]
	s_and_saveexec_b64 s[10:11], s[0:1]
	s_cbranch_execz .LBB0_665
	global_load_ushort v37, v[6:7], off offset:16
.LBB0_665:
	s_or_b64 exec, exec, s[10:11]
	v_add_u32_e32 v35, 0xa00, v1
	v_ashrrev_i32_e32 v2, 1, v35
	v_and_b32_e32 v2, 0xfffffe00, v2
	v_add_u32_e32 v2, s38, v2
	v_mov_b64_e32 v[6:7], s[20:21]
	v_mad_i64_i32 v[6:7], s[10:11], v2, s22, v[6:7]
	v_lshlrev_b32_e32 v2, 4, v35
	v_and_b32_e32 v2, 0x2000, v2
	v_lshl_add_u64 v[6:7], v[6:7], 0, v[2:3]
	v_mov_b32_e32 v5, v3
	v_lshl_add_u64 v[56:57], v[6:7], 0, v[4:5]
	global_load_dwordx4 v[4:7], v[56:57], off
	v_mov_b32_e32 v33, 0
	v_mov_b32_e32 v34, 0
	s_and_saveexec_b64 s[10:11], vcc
	s_cbranch_execz .LBB0_667
	global_load_ushort v34, v[56:57], off offset:-2
.LBB0_667:
	s_or_b64 exec, exec, s[10:11]
	s_and_saveexec_b64 s[10:11], s[0:1]
	s_cbranch_execz .LBB0_669
	global_load_ushort v33, v[56:57], off offset:16
.LBB0_669:
	s_or_b64 exec, exec, s[10:11]
	v_ashrrev_i32_e32 v56, 10, v1
	v_lshlrev_b32_e32 v36, 9, v56
	v_add_u32_e32 v62, s46, v36
	v_ashrrev_i32_e32 v63, 31, v62
	s_add_i32 s11, s46, 0x600
	v_lshl_add_u64 v[62:63], v[62:63], 2, s[4:5]
	global_load_dword v2, v[62:63], off
	v_add_u32_e32 v62, s11, v36
	v_ashrrev_i32_e32 v63, 31, v62
	s_add_i32 s10, s46, 0xc00
	v_lshl_add_u64 v[62:63], v[62:63], 2, s[4:5]
	global_load_dword v32, v[62:63], off
	v_add_u32_e32 v62, s10, v36
	v_ashrrev_i32_e32 v63, 31, v62
	v_lshl_add_u64 v[62:63], v[62:63], 2, s[4:5]
	global_load_dword v36, v[62:63], off
	s_waitcnt vmcnt(3)
	v_lshlrev_b32_e32 v54, 16, v54
	v_lshlrev_b32_e32 v53, 16, v53
	v_lshlrev_b32_e32 v50, 16, v50
	v_lshlrev_b32_e32 v49, 16, v49
	v_lshlrev_b32_e32 v46, 16, v46
	v_lshlrev_b32_e32 v45, 16, v45
	v_lshlrev_b32_e32 v42, 16, v42
	v_lshlrev_b32_e32 v41, 16, v41
	v_lshlrev_b32_e32 v38, 16, v38
	v_lshlrev_b32_e32 v37, 16, v37
	v_lshlrev_b32_e32 v34, 16, v34
	v_lshlrev_b32_e32 v33, 16, v33
	v_bfe_u32 v62, v1, 9, 1
	v_cmp_lt_u32_e32 vcc, s23, v1
	s_and_saveexec_b64 s[0:1], vcc
	s_xor_b64 s[0:1], exec, s[0:1]
	s_cbranch_execz .LBB0_671
	s_mov_b64 s[38:39], src_shared_base
	s_cmp_lg_u32 0, -1
	s_cselect_b32 s38, 0, 0
	s_cselect_b32 s39, s39, 0
	s_add_u32 s38, s38, 0x1a1a0
	s_addc_u32 s39, s39, 0
	s_cmp_lg_u64 s[38:39], 0
	s_cselect_b32 s38, s38, -1
	s_add_i32 s39, 0, 0x1e1a0
	v_mov_b32_e32 v40, s39
	v_mov_b32_e32 v43, s38
	v_cmp_eq_u32_e32 vcc, 1, v56
	s_nop 1
	v_cndmask_b32_e32 v40, v40, v43, vcc
	v_lshl_add_u32 v40, v62, 13, v40

.LBB0_1417:
	v_lshrrev_b32_e32 v20, 1, v10
	v_and_b32_e32 v20, 24, v20
	v_and_b32_e32 v11, 15, v10
	v_lshlrev_b32_e32 v21, 1, v20
	v_lshlrev_b32_e32 v10, 2, v10
	s_lshl_b32 s1, s1, 5
	v_lshl_or_b32 v1, s10, 6, v11
	s_lshl_b32 s10, s10, 13
	v_lshl_or_b32 v11, v11, 6, v21
	v_and_b32_e32 v10, 32, v10
	s_and_b32 s1, s1, 0x60
	v_lshl_add_u64 v[12:13], s[52:53], 0, v[2:3]
	v_mov_b32_e32 v133, v3
	v_readlane_b32 s48, v254, 14
	v_bitop3_b32 v21, v11, s10, v10 bitop3:0xde
	s_lshl_b32 s10, s1, 7
	v_lshl_add_u64 v[14:15], s[52:53], 0, v[132:133]
	v_mov_b32_e32 v137, v3
	v_readlane_b32 s49, v254, 15
	v_bitop3_b32 v142, v11, s10, v10 bitop3:0xde
	s_add_i32 m0, s58, 0x18000
	v_lshl_add_u64 v[10:11], v[12:13], 0, s[6:7]
	v_lshl_add_u64 v[16:17], s[48:49], 0, v[136:137]
	v_mov_b32_e32 v135, v3
	s_waitcnt vmcnt(2)
	s_barrier
	global_load_lds_dwordx4 v[10:11], off
	v_lshl_add_u64 v[10:11], v[14:15], 0, s[6:7]
	s_add_i32 m0, s58, 0x1a000
	s_add_i32 s62, s58, 0x8000
	s_add_i32 s63, s58, 0xa000
	v_lshl_add_u64 v[18:19], s[48:49], 0, v[134:135]
	global_load_lds_dwordx4 v[10:11], off
	v_lshl_add_u64 v[10:11], v[16:17], 0, s[6:7]
	s_mov_b32 m0, s62
	s_add_u32 s10, s52, 0x80080
	global_load_lds_dwordx4 v[10:11], off
	v_lshl_add_u64 v[10:11], v[18:19], 0, s[6:7]
	s_mov_b32 m0, s63
	s_addc_u32 s11, s53, 0
	global_load_lds_dwordx4 v[10:11], off
	s_add_i32 m0, s58, 0x1c000
	v_lshl_add_u64 v[10:11], s[10:11], 0, v[2:3]
	global_load_lds_dwordx4 v[10:11], off
	v_lshl_add_u64 v[10:11], s[10:11], 0, v[132:133]
	s_add_i32 m0, s58, 0x1e000
	s_cmpk_lt_u32 s0, 0x100
	global_load_lds_dwordx4 v[10:11], off
	v_lshlrev_b32_e32 v10, 15, v8
	v_and_b32_e32 v10, 0xffff0000, v10
	v_lshl_add_u32 v7, v7, 12, v10
	v_and_b32_e32 v8, 1, v8
	v_lshl_or_b32 v7, v8, 6, v7
	v_lshl_add_u32 v138, v9, 1, v7
	v_lshlrev_b32_e32 v7, 15, v4
	v_and_b32_e32 v7, 0xffff0000, v7
	s_waitcnt vmcnt(6)
	v_lshl_add_u32 v5, v5, 12, v7
	v_and_b32_e32 v4, 1, v4
	v_or_b32_e32 v144, s1, v20
	v_lshl_or_b32 v4, v4, 6, v5
	v_readlane_b32 s0, v254, 20
	v_or_b32_e32 v143, 0x400, v142
	v_add_u32_e32 v142, 0x10000, v142
	s_cselect_b64 s[36:37], -1, 0
	v_mov_b32_e32 v139, v3
	v_lshl_add_u32 v140, v6, 1, v4
	v_mov_b32_e32 v141, v3
	s_mov_b32 s64, 0
	v_add_u32_e32 v145, 0, v21
	v_readlane_b32 s65, v254, 9
	s_mov_b32 s66, s0
	s_barrier
	v_readlane_b32 s1, v254, 21
	s_branch .LBB0_1420

.LBB0_1427:
	s_add_u32 s42, s48, 0xfff80080
	s_addc_u32 s43, s49, -1
	s_add_i32 s70, 0, 0x10000
	s_cmp_eq_u32 s69, 28
	s_cselect_b32 s55, s10, s43
	s_cselect_b32 s54, s11, s42
	s_cselect_b32 s53, s39, s68
	s_cselect_b32 s52, s41, s67
	s_add_i32 s71, 0, 0x14000
	ds_read_b128 v[146:149], v142
	ds_read_b128 v[150:153], v142 offset:1024
	ds_read_b128 v[154:157], v142 offset:2048
	ds_read_b128 v[158:161], v142 offset:3072
	ds_read_b128 v[162:165], v142 offset:16384
	ds_read_b128 v[166:169], v142 offset:17408
	ds_read_b128 v[170:173], v142 offset:18432
	ds_read_b128 v[178:181], v142 offset:19456
	v_lshl_add_u64 v[174:175], s[48:49], 0, v[138:139]
	s_add_i32 m0, s58, 0xc000
	ds_read_b128 v[182:185], v145
	ds_read_b128 v[186:189], v145 offset:1024
	ds_read_b128 v[190:193], v145 offset:2048
	ds_read_b128 v[194:197], v145 offset:3072
	ds_read_b128 v[198:201], v145 offset:4096
	ds_read_b128 v[202:205], v145 offset:5120
	ds_read_b128 v[206:209], v145 offset:6144
	ds_read_b128 v[226:229], v145 offset:7168
	global_load_lds_dwordx4 v[174:175], off
	v_lshl_add_u64 v[174:175], s[48:49], 0, v[140:141]
	s_add_i32 m0, s58, 0xe000
	s_nop 0
	global_load_lds_dwordx4 v[174:175], off
	s_waitcnt vmcnt(8)
	s_waitcnt lgkmcnt(0)
	s_barrier
	s_setprio 1
	s_waitcnt lgkmcnt(0)
	v_mfma_f32_16x16x32_bf16 v[128:131], v[146:149], v[182:185], v[128:131]
	v_mfma_f32_16x16x32_bf16 v[124:127], v[154:157], v[182:185], v[124:127]
	v_mfma_f32_16x16x32_bf16 v[120:123], v[146:149], v[190:193], v[120:123]
	v_mfma_f32_16x16x32_bf16 v[116:119], v[154:157], v[190:193], v[116:119]
	v_mfma_f32_16x16x32_bf16 v[104:107], v[146:149], v[198:201], v[104:107]
	v_mfma_f32_16x16x32_bf16 v[100:103], v[154:157], v[198:201], v[100:103]
	v_mfma_f32_16x16x32_bf16 v[88:91], v[146:149], v[206:209], v[88:91]
	v_mfma_f32_16x16x32_bf16 v[84:87], v[154:157], v[206:209], v[84:87]
	v_mfma_f32_16x16x32_bf16 v[128:131], v[150:153], v[186:189], v[128:131]
	v_mfma_f32_16x16x32_bf16 v[124:127], v[158:161], v[186:189], v[124:127]
	v_mfma_f32_16x16x32_bf16 v[120:123], v[150:153], v[194:197], v[120:123]
	v_mfma_f32_16x16x32_bf16 v[116:119], v[158:161], v[194:197], v[116:119]
	v_mfma_f32_16x16x32_bf16 v[104:107], v[150:153], v[202:205], v[104:107]
	v_mfma_f32_16x16x32_bf16 v[100:103], v[158:161], v[202:205], v[100:103]
	v_mfma_f32_16x16x32_bf16 v[88:91], v[150:153], v[226:229], v[88:91]
	v_mfma_f32_16x16x32_bf16 v[84:87], v[158:161], v[226:229], v[84:87]
	s_setprio 0
	s_setprio 1
	v_mfma_f32_16x16x32_bf16 v[112:115], v[162:165], v[182:185], v[112:115]
	v_mfma_f32_16x16x32_bf16 v[108:111], v[170:173], v[182:185], v[108:111]
	v_mfma_f32_16x16x32_bf16 v[96:99], v[162:165], v[190:193], v[96:99]
	v_mfma_f32_16x16x32_bf16 v[92:95], v[170:173], v[190:193], v[92:95]
	v_mfma_f32_16x16x32_bf16 v[80:83], v[162:165], v[198:201], v[80:83]
	v_mfma_f32_16x16x32_bf16 v[76:79], v[170:173], v[198:201], v[76:79]
	v_mfma_f32_16x16x32_bf16 v[72:75], v[162:165], v[206:209], v[72:75]
	v_mfma_f32_16x16x32_bf16 v[68:71], v[170:173], v[206:209], v[68:71]
	v_mfma_f32_16x16x32_bf16 v[112:115], v[166:169], v[186:189], v[112:115]
	v_mfma_f32_16x16x32_bf16 v[108:111], v[178:181], v[186:189], v[108:111]
	v_mfma_f32_16x16x32_bf16 v[96:99], v[166:169], v[194:197], v[96:99]
	v_mfma_f32_16x16x32_bf16 v[92:95], v[178:181], v[194:197], v[92:95]
	v_mfma_f32_16x16x32_bf16 v[80:83], v[166:169], v[202:205], v[80:83]
	v_mfma_f32_16x16x32_bf16 v[76:79], v[178:181], v[202:205], v[76:79]
	v_mfma_f32_16x16x32_bf16 v[72:75], v[166:169], v[226:229], v[72:75]
	v_mfma_f32_16x16x32_bf16 v[68:71], v[178:181], v[226:229], v[68:71]
	s_setprio 0
	s_barrier
	s_add_i32 s42, s70, s57
	v_lshl_add_u64 v[174:175], s[52:53], 0, v[2:3]
	s_mov_b32 m0, s42
	ds_read_b128 v[182:185], v145 offset:16384
	ds_read_b128 v[186:189], v145 offset:17408
	ds_read_b128 v[190:193], v145 offset:18432
	ds_read_b128 v[194:197], v145 offset:19456
	ds_read_b128 v[198:201], v145 offset:20480
	ds_read_b128 v[202:205], v145 offset:21504
	ds_read_b128 v[206:209], v145 offset:22528
	ds_read_b128 v[226:229], v145 offset:23552
	global_load_lds_dwordx4 v[174:175], off
	s_add_i32 m0, s42, 0x2000
	s_add_u32 s42, s52, 0x80000
	v_lshl_add_u64 v[210:211], s[52:53], 0, v[132:133]
	s_addc_u32 s43, s53, 0
	s_add_i32 s70, s71, s57
	global_load_lds_dwordx4 v[210:211], off
	v_lshl_add_u64 v[214:215], s[42:43], 0, v[2:3]
	s_mov_b32 m0, s70
	v_lshl_add_u64 v[230:231], s[54:55], 0, v[134:135]
	global_load_lds_dwordx4 v[214:215], off
	v_lshl_add_u64 v[214:215], s[42:43], 0, v[132:133]
	s_add_i32 m0, s70, 0x2000
	s_nop 0
	global_load_lds_dwordx4 v[214:215], off
	v_lshl_add_u64 v[214:215], s[54:55], 0, v[136:137]
	s_mov_b32 m0, s58
	s_nop 0
	global_load_lds_dwordx4 v[214:215], off
	s_mov_b32 m0, s59
	s_nop 0
	global_load_lds_dwordx4 v[230:231], off
	s_waitcnt vmcnt(8)
	s_waitcnt lgkmcnt(0)
	s_barrier
	s_setprio 1
	s_waitcnt lgkmcnt(0)
	v_mfma_f32_16x16x32_bf16 v[64:67], v[146:149], v[182:185], v[64:67]
	v_mfma_f32_16x16x32_bf16 v[60:63], v[154:157], v[182:185], v[60:63]
	v_mfma_f32_16x16x32_bf16 v[56:59], v[146:149], v[190:193], v[56:59]
	v_mfma_f32_16x16x32_bf16 v[52:55], v[154:157], v[190:193], v[52:55]
	v_mfma_f32_16x16x32_bf16 v[40:43], v[146:149], v[198:201], v[40:43]
	v_mfma_f32_16x16x32_bf16 v[36:39], v[154:157], v[198:201], v[36:39]
	v_mfma_f32_16x16x32_bf16 v[24:27], v[146:149], v[206:209], v[24:27]
	v_mfma_f32_16x16x32_bf16 v[20:23], v[154:157], v[206:209], v[20:23]
	v_mfma_f32_16x16x32_bf16 v[64:67], v[150:153], v[186:189], v[64:67]
	v_mfma_f32_16x16x32_bf16 v[60:63], v[158:161], v[186:189], v[60:63]
	v_mfma_f32_16x16x32_bf16 v[56:59], v[150:153], v[194:197], v[56:59]
	v_mfma_f32_16x16x32_bf16 v[52:55], v[158:161], v[194:197], v[52:55]
	v_mfma_f32_16x16x32_bf16 v[40:43], v[150:153], v[202:205], v[40:43]
	v_mfma_f32_16x16x32_bf16 v[36:39], v[158:161], v[202:205], v[36:39]
	v_mfma_f32_16x16x32_bf16 v[24:27], v[150:153], v[226:229], v[24:27]
	v_mfma_f32_16x16x32_bf16 v[20:23], v[158:161], v[226:229], v[20:23]
	s_setprio 0
	s_setprio 1
	v_mfma_f32_16x16x32_bf16 v[48:51], v[162:165], v[182:185], v[48:51]
	v_mfma_f32_16x16x32_bf16 v[44:47], v[170:173], v[182:185], v[44:47]
	v_mfma_f32_16x16x32_bf16 v[32:35], v[162:165], v[190:193], v[32:35]
	v_mfma_f32_16x16x32_bf16 v[28:31], v[170:173], v[190:193], v[28:31]
	v_mfma_f32_16x16x32_bf16 v[16:19], v[162:165], v[198:201], v[16:19]
	v_mfma_f32_16x16x32_bf16 v[12:15], v[170:173], v[198:201], v[12:15]
	v_mfma_f32_16x16x32_bf16 v[8:11], v[162:165], v[206:209], v[8:11]
	v_mfma_f32_16x16x32_bf16 v[4:7], v[170:173], v[206:209], v[4:7]
	v_mfma_f32_16x16x32_bf16 v[48:51], v[166:169], v[186:189], v[48:51]
	v_mfma_f32_16x16x32_bf16 v[44:47], v[178:181], v[186:189], v[44:47]
	v_mfma_f32_16x16x32_bf16 v[32:35], v[166:169], v[194:197], v[32:35]
	v_mfma_f32_16x16x32_bf16 v[28:31], v[178:181], v[194:197], v[28:31]
	v_mfma_f32_16x16x32_bf16 v[16:19], v[166:169], v[202:205], v[16:19]
	v_mfma_f32_16x16x32_bf16 v[12:15], v[178:181], v[202:205], v[12:15]
	v_mfma_f32_16x16x32_bf16 v[8:11], v[166:169], v[226:229], v[8:11]
	v_mfma_f32_16x16x32_bf16 v[4:7], v[178:181], v[226:229], v[4:7]
	s_setprio 0
	s_barrier
	s_add_i32 s70, 0, 0x18000
	s_add_i32 s71, 0, 0x1c000
	ds_read_b128 v[146:149], v142 offset:32768
	ds_read_b128 v[150:153], v142 offset:33792
	ds_read_b128 v[154:157], v142 offset:34816
	ds_read_b128 v[158:161], v142 offset:35840
	ds_read_b128 v[162:165], v142 offset:49152
	ds_read_b128 v[166:169], v142 offset:50176
	ds_read_b128 v[170:173], v142 offset:51200
	ds_read_b128 v[178:181], v142 offset:52224
	s_add_u32 s42, s54, 0x80000
	s_addc_u32 s43, s55, 0
	s_mov_b32 m0, s60
	v_lshl_add_u64 v[232:233], s[42:43], 0, v[136:137]
	ds_read_b128 v[182:185], v145 offset:32768
	ds_read_b128 v[186:189], v145 offset:33792
	ds_read_b128 v[190:193], v145 offset:34816
	ds_read_b128 v[194:197], v145 offset:35840
	ds_read_b128 v[198:201], v145 offset:36864
	ds_read_b128 v[202:205], v145 offset:37888
	ds_read_b128 v[206:209], v145 offset:38912
	ds_read_b128 v[226:229], v145 offset:39936
	global_load_lds_dwordx4 v[232:233], off
	v_lshl_add_u64 v[232:233], s[42:43], 0, v[134:135]
	s_mov_b32 m0, s61
	s_nop 0
	global_load_lds_dwordx4 v[232:233], off
	s_waitcnt vmcnt(8)
	s_waitcnt lgkmcnt(0)
	s_barrier
	s_setprio 1
	s_waitcnt lgkmcnt(0)
	v_mfma_f32_16x16x32_bf16 v[128:131], v[146:149], v[182:185], v[128:131]
	v_mfma_f32_16x16x32_bf16 v[124:127], v[154:157], v[182:185], v[124:127]
	v_mfma_f32_16x16x32_bf16 v[120:123], v[146:149], v[190:193], v[120:123]
	v_mfma_f32_16x16x32_bf16 v[116:119], v[154:157], v[190:193], v[116:119]
	v_mfma_f32_16x16x32_bf16 v[104:107], v[146:149], v[198:201], v[104:107]
	v_mfma_f32_16x16x32_bf16 v[100:103], v[154:157], v[198:201], v[100:103]
	v_mfma_f32_16x16x32_bf16 v[88:91], v[146:149], v[206:209], v[88:91]
	v_mfma_f32_16x16x32_bf16 v[84:87], v[154:157], v[206:209], v[84:87]
	v_mfma_f32_16x16x32_bf16 v[128:131], v[150:153], v[186:189], v[128:131]
	v_mfma_f32_16x16x32_bf16 v[124:127], v[158:161], v[186:189], v[124:127]
	v_mfma_f32_16x16x32_bf16 v[120:123], v[150:153], v[194:197], v[120:123]
	v_mfma_f32_16x16x32_bf16 v[116:119], v[158:161], v[194:197], v[116:119]
	v_mfma_f32_16x16x32_bf16 v[104:107], v[150:153], v[202:205], v[104:107]
	v_mfma_f32_16x16x32_bf16 v[100:103], v[158:161], v[202:205], v[100:103]
	v_mfma_f32_16x16x32_bf16 v[88:91], v[150:153], v[226:229], v[88:91]
	v_mfma_f32_16x16x32_bf16 v[84:87], v[158:161], v[226:229], v[84:87]
	s_setprio 0
	s_setprio 1
	v_mfma_f32_16x16x32_bf16 v[112:115], v[162:165], v[182:185], v[112:115]
	v_mfma_f32_16x16x32_bf16 v[108:111], v[170:173], v[182:185], v[108:111]
	v_mfma_f32_16x16x32_bf16 v[96:99], v[162:165], v[190:193], v[96:99]
	v_mfma_f32_16x16x32_bf16 v[92:95], v[170:173], v[190:193], v[92:95]
	v_mfma_f32_16x16x32_bf16 v[80:83], v[162:165], v[198:201], v[80:83]
	v_mfma_f32_16x16x32_bf16 v[76:79], v[170:173], v[198:201], v[76:79]
	v_mfma_f32_16x16x32_bf16 v[72:75], v[162:165], v[206:209], v[72:75]
	v_mfma_f32_16x16x32_bf16 v[68:71], v[170:173], v[206:209], v[68:71]
	v_mfma_f32_16x16x32_bf16 v[112:115], v[166:169], v[186:189], v[112:115]
	v_mfma_f32_16x16x32_bf16 v[108:111], v[178:181], v[186:189], v[108:111]
	v_mfma_f32_16x16x32_bf16 v[96:99], v[166:169], v[194:197], v[96:99]
	v_mfma_f32_16x16x32_bf16 v[92:95], v[178:181], v[194:197], v[92:95]
	v_mfma_f32_16x16x32_bf16 v[80:83], v[166:169], v[202:205], v[80:83]
	v_mfma_f32_16x16x32_bf16 v[76:79], v[178:181], v[202:205], v[76:79]
	v_mfma_f32_16x16x32_bf16 v[72:75], v[166:169], v[226:229], v[72:75]
	v_mfma_f32_16x16x32_bf16 v[68:71], v[178:181], v[226:229], v[68:71]
	s_setprio 0
	s_barrier
	s_add_i32 s42, s70, s57
	v_lshl_add_u64 v[174:175], v[174:175], 0, s[6:7]
	s_mov_b32 m0, s42
	ds_read_b128 v[182:185], v145 offset:49152
	ds_read_b128 v[186:189], v145 offset:50176
	ds_read_b128 v[190:193], v145 offset:51200
	ds_read_b128 v[194:197], v145 offset:52224
	ds_read_b128 v[198:201], v145 offset:53248
	ds_read_b128 v[202:205], v145 offset:54272
	ds_read_b128 v[206:209], v145 offset:55296
	ds_read_b128 v[226:229], v145 offset:56320
	global_load_lds_dwordx4 v[174:175], off
	s_add_i32 m0, s42, 0x2000
	s_add_u32 s42, s52, 0x80080
	v_lshl_add_u64 v[174:175], v[210:211], 0, s[6:7]
	s_addc_u32 s43, s53, 0
	s_add_i32 s52, s71, s57
	global_load_lds_dwordx4 v[174:175], off
	v_lshl_add_u64 v[174:175], s[42:43], 0, v[2:3]
	s_mov_b32 m0, s52
	s_nop 0
	global_load_lds_dwordx4 v[174:175], off
	v_lshl_add_u64 v[174:175], s[42:43], 0, v[132:133]
	s_add_i32 m0, s52, 0x2000
	s_nop 0
	global_load_lds_dwordx4 v[174:175], off
	v_lshl_add_u64 v[174:175], v[214:215], 0, s[6:7]
	s_mov_b32 m0, s62
	s_nop 0
	global_load_lds_dwordx4 v[174:175], off
	v_lshl_add_u64 v[174:175], v[230:231], 0, s[6:7]
	s_mov_b32 m0, s63
	s_nop 0
	global_load_lds_dwordx4 v[174:175], off
	s_waitcnt vmcnt(8)
	s_waitcnt lgkmcnt(0)
	s_barrier
	s_setprio 1
	s_waitcnt lgkmcnt(0)
	v_mfma_f32_16x16x32_bf16 v[64:67], v[146:149], v[182:185], v[64:67]
	v_mfma_f32_16x16x32_bf16 v[60:63], v[154:157], v[182:185], v[60:63]
	v_mfma_f32_16x16x32_bf16 v[56:59], v[146:149], v[190:193], v[56:59]
	v_mfma_f32_16x16x32_bf16 v[52:55], v[154:157], v[190:193], v[52:55]
	v_mfma_f32_16x16x32_bf16 v[40:43], v[146:149], v[198:201], v[40:43]
	v_mfma_f32_16x16x32_bf16 v[36:39], v[154:157], v[198:201], v[36:39]
	v_mfma_f32_16x16x32_bf16 v[24:27], v[146:149], v[206:209], v[24:27]
	v_mfma_f32_16x16x32_bf16 v[20:23], v[154:157], v[206:209], v[20:23]
	v_mfma_f32_16x16x32_bf16 v[64:67], v[150:153], v[186:189], v[64:67]
	v_mfma_f32_16x16x32_bf16 v[60:63], v[158:161], v[186:189], v[60:63]
	v_mfma_f32_16x16x32_bf16 v[56:59], v[150:153], v[194:197], v[56:59]
	v_mfma_f32_16x16x32_bf16 v[52:55], v[158:161], v[194:197], v[52:55]
	v_mfma_f32_16x16x32_bf16 v[40:43], v[150:153], v[202:205], v[40:43]
	v_mfma_f32_16x16x32_bf16 v[36:39], v[158:161], v[202:205], v[36:39]
	v_mfma_f32_16x16x32_bf16 v[24:27], v[150:153], v[226:229], v[24:27]
	v_mfma_f32_16x16x32_bf16 v[20:23], v[158:161], v[226:229], v[20:23]
	s_setprio 0
	s_setprio 1
	v_mfma_f32_16x16x32_bf16 v[48:51], v[162:165], v[182:185], v[48:51]
	v_mfma_f32_16x16x32_bf16 v[44:47], v[170:173], v[182:185], v[44:47]
	v_mfma_f32_16x16x32_bf16 v[32:35], v[162:165], v[190:193], v[32:35]
	v_mfma_f32_16x16x32_bf16 v[28:31], v[170:173], v[190:193], v[28:31]
	v_mfma_f32_16x16x32_bf16 v[16:19], v[162:165], v[198:201], v[16:19]
	v_mfma_f32_16x16x32_bf16 v[12:15], v[170:173], v[198:201], v[12:15]
	v_mfma_f32_16x16x32_bf16 v[8:11], v[162:165], v[206:209], v[8:11]
	v_mfma_f32_16x16x32_bf16 v[4:7], v[170:173], v[206:209], v[4:7]
	v_mfma_f32_16x16x32_bf16 v[48:51], v[166:169], v[186:189], v[48:51]
	v_mfma_f32_16x16x32_bf16 v[44:47], v[178:181], v[186:189], v[44:47]
	v_mfma_f32_16x16x32_bf16 v[32:35], v[166:169], v[194:197], v[32:35]
	v_mfma_f32_16x16x32_bf16 v[28:31], v[178:181], v[194:197], v[28:31]
	v_mfma_f32_16x16x32_bf16 v[16:19], v[166:169], v[202:205], v[16:19]
	v_mfma_f32_16x16x32_bf16 v[12:15], v[178:181], v[202:205], v[12:15]
	v_mfma_f32_16x16x32_bf16 v[8:11], v[166:169], v[226:229], v[8:11]
	v_mfma_f32_16x16x32_bf16 v[4:7], v[178:181], v[226:229], v[4:7]
	s_setprio 0
	s_barrier
	s_add_i32 s69, s69, 2
	s_add_u32 s48, s48, 0x100
	s_addc_u32 s49, s49, 0
	s_add_u32 s67, s67, 0x100
	s_addc_u32 s68, s68, 0
	s_cmp_gt_u32 s69, 29
	s_cbranch_scc0 .LBB0_1427
	s_and_b64 vcc, exec, s[36:37]
	s_cbranch_vccz .LBB0_1430
	s_barrier

.LBB0_1766:
	v_lshrrev_b32_e32 v19, 4, v18
	v_and_b32_e32 v20, 15, v18
	s_lshl_b32 s1, s1, 5
	v_lshl_or_b32 v1, s10, 6, v20
	v_bfe_u32 v19, v19, 1, 1
	s_lshl_b32 s10, s10, 13
	s_and_b32 s1, s1, 0x60
	s_add_i32 m0, s47, 0x18000
	v_lshl_add_u64 v[10:11], v[10:11], 0, s[6:7]
	v_lshl_or_b32 v24, v19, 10, s10
	s_lshr_b32 s10, s1, 3
	s_waitcnt vmcnt(2)
	s_barrier
	global_load_lds_dwordx4 v[10:11], off
	v_lshl_add_u64 v[8:9], v[8:9], 0, s[6:7]
	s_add_i32 m0, s47, 0x1a000
	s_add_i32 s63, s47, 0x8000
	s_add_i32 s64, s47, 0xa000
	v_or_b32_e32 v19, s10, v19
	global_load_lds_dwordx4 v[8:9], off
	v_lshl_add_u64 v[4:5], v[4:5], 0, s[6:7]
	s_mov_b32 m0, s63
	s_add_u32 s10, s52, 0x40080
	global_load_lds_dwordx4 v[4:5], off
	v_lshl_add_u64 v[4:5], v[6:7], 0, s[6:7]
	s_mov_b32 m0, s64
	s_addc_u32 s11, s53, 0
	global_load_lds_dwordx4 v[4:5], off
	s_add_i32 m0, s47, 0x1c000
	v_lshl_add_u64 v[4:5], s[10:11], 0, v[2:3]
	global_load_lds_dwordx4 v[4:5], off
	v_lshl_add_u64 v[4:5], s[10:11], 0, v[164:165]
	s_add_i32 m0, s47, 0x1e000
	v_lshlrev_b32_e32 v22, 1, v18
	global_load_lds_dwordx4 v[4:5], off
	v_lshlrev_b32_e32 v4, 14, v16
	v_and_b32_e32 v4, 0xffff8000, v4
	v_lshl_add_u32 v4, v15, 11, v4
	v_and_b32_e32 v5, 1, v16
	v_lshl_or_b32 v4, v5, 6, v4
	v_bfe_u32 v21, v18, 4, 2
	v_and_b32_e32 v22, 32, v22
	v_lshlrev_b32_e32 v20, 6, v20
	v_lshlrev_b32_e32 v18, 2, v18
	v_lshl_add_u32 v170, v17, 1, v4
	v_lshlrev_b32_e32 v4, 14, v12
	v_or_b32_e32 v23, v20, v22
	v_and_b32_e32 v18, 32, v18
	v_and_b32_e32 v4, 0xffff8000, v4
	v_bitop3_b32 v20, v20, v18, v22 bitop3:0x36
	v_bitop3_b32 v25, v23, v18, 16 bitop3:0x36
	s_waitcnt vmcnt(6)
	v_lshl_add_u32 v4, v13, 11, v4
	v_and_b32_e32 v5, 1, v12
	v_or_b32_e32 v20, v20, v24
	v_or_b32_e32 v22, 16, v23
	v_or_b32_e32 v24, v25, v24
	v_lshlrev_b32_e32 v19, 10, v19
	s_cmpk_lt_u32 s0, 0x100
	v_lshl_or_b32 v4, v5, 6, v4
	v_bitop3_b32 v190, v19, v23, v18 bitop3:0xf6
	v_bitop3_b32 v191, v22, v19, v18 bitop3:0xde
	s_cselect_b64 s[14:15], -1, 0
	v_lshl_or_b32 v192, v21, 3, s1
	v_mov_b32_e32 v171, v3
	v_lshl_add_u32 v172, v14, 1, v4
	v_mov_b32_e32 v173, v3
	s_mov_b32 s65, 0
	v_add_u32_e32 v193, 0, v20
	v_add_u32_e32 v194, 0, v24
	v_and_b32_e32 v193, 15, v0
	v_lshlrev_b32_e32 v193, 6, v193
	v_bfe_u32 v194, v0, 4, 2
	v_lshl_or_b32 v193, v194, 4, v193
	v_and_b32_e32 v194, 8, v0
	v_lshlrev_b32_e32 v194, 2, v194
	v_xor_b32_e32 v193, v193, v194
	v_bfe_u32 v190, v0, 6, 2
	v_lshl_or_b32 v190, v190, 12, v193
	v_or_b32_e32 v191, 0x400, v190
	v_add_u32_e32 v190, 0x10000, v190
	v_lshrrev_b32_e32 v194, 8, v0
	v_lshl_or_b32 v193, v194, 13, v193
	v_or_b32_e32 v194, 0x400, v193
	s_barrier
	s_branch .LBB0_1769

.LBB0_1772:
	s_add_u32 s43, s50, 0xfffc0080
	s_addc_u32 s52, s51, -1
	s_add_i32 s42, 0, 0x10000
	s_cmp_eq_u32 s68, 12
	s_cselect_b32 s55, s10, s52
	s_cselect_b32 s54, s11, s43
	s_cselect_b32 s53, s37, s67
	s_cselect_b32 s52, s39, s66
	s_add_i32 s43, 0, 0x14000
	ds_read_b128 v[20:23], v190
	ds_read_b128 v[28:31], v190 offset:2048
	ds_read_b128 v[24:27], v190 offset:1024
	ds_read_b128 v[32:35], v190 offset:3072
	ds_read_b128 v[4:7], v190 offset:16384
	ds_read_b128 v[12:15], v190 offset:18432
	ds_read_b128 v[8:11], v190 offset:17408
	ds_read_b128 v[16:19], v190 offset:19456
	v_lshl_add_u64 v[174:175], s[50:51], 0, v[170:171]
	s_add_i32 m0, s47, 0xc000
	ds_read_b128 v[178:181], v193
	ds_read_b128 v[196:199], v193 offset:2048
	ds_read_b128 v[182:185], v194
	ds_read_b128 v[200:203], v194 offset:2048
	ds_read_b128 v[204:207], v193 offset:4096
	ds_read_b128 v[226:229], v193 offset:6144
	ds_read_b128 v[208:211], v194 offset:4096
	ds_read_b128 v[230:233], v194 offset:6144
	global_load_lds_dwordx4 v[174:175], off
	v_lshl_add_u64 v[174:175], s[50:51], 0, v[172:173]
	s_add_i32 m0, s47, 0xe000
	s_nop 0
	global_load_lds_dwordx4 v[174:175], off
	s_waitcnt vmcnt(8)
	s_waitcnt lgkmcnt(0)
	s_barrier
	s_setprio 1
	s_waitcnt lgkmcnt(0)
	v_mfma_scale_f32_16x16x128_f8f6f4 v[160:163], v[20:27], v[178:185], v[160:163], v219, v220 op_sel_hi:[0,0,0]
	v_mfma_scale_f32_16x16x128_f8f6f4 v[152:155], v[28:35], v[178:185], v[152:155], v219, v220 op_sel_hi:[0,0,0]
	v_mfma_scale_f32_16x16x128_f8f6f4 v[144:147], v[20:27], v[196:203], v[144:147], v219, v220 op_sel_hi:[0,0,0]
	v_mfma_scale_f32_16x16x128_f8f6f4 v[136:139], v[28:35], v[196:203], v[136:139], v219, v220 op_sel_hi:[0,0,0]
	v_mfma_scale_f32_16x16x128_f8f6f4 v[128:131], v[20:27], v[204:211], v[128:131], v219, v220 op_sel_hi:[0,0,0]
	v_mfma_scale_f32_16x16x128_f8f6f4 v[120:123], v[28:35], v[204:211], v[120:123], v219, v220 op_sel_hi:[0,0,0]
	v_mfma_scale_f32_16x16x128_f8f6f4 v[112:115], v[20:27], v[226:233], v[112:115], v219, v220 op_sel_hi:[0,0,0]
	v_mfma_scale_f32_16x16x128_f8f6f4 v[104:107], v[28:35], v[226:233], v[104:107], v219, v220 op_sel_hi:[0,0,0]
	s_setprio 0
	s_setprio 1
	v_mfma_scale_f32_16x16x128_f8f6f4 v[156:159], v[4:11], v[178:185], v[156:159], v219, v220 op_sel_hi:[0,0,0]
	v_mfma_scale_f32_16x16x128_f8f6f4 v[148:151], v[12:19], v[178:185], v[148:151], v219, v220 op_sel_hi:[0,0,0]
	v_mfma_scale_f32_16x16x128_f8f6f4 v[140:143], v[4:11], v[196:203], v[140:143], v219, v220 op_sel_hi:[0,0,0]
	v_mfma_scale_f32_16x16x128_f8f6f4 v[132:135], v[12:19], v[196:203], v[132:135], v219, v220 op_sel_hi:[0,0,0]
	v_mfma_scale_f32_16x16x128_f8f6f4 v[124:127], v[4:11], v[204:211], v[124:127], v219, v220 op_sel_hi:[0,0,0]
	v_mfma_scale_f32_16x16x128_f8f6f4 v[116:119], v[12:19], v[204:211], v[116:119], v219, v220 op_sel_hi:[0,0,0]
	v_mfma_scale_f32_16x16x128_f8f6f4 v[108:111], v[4:11], v[226:233], v[108:111], v219, v220 op_sel_hi:[0,0,0]
	v_mfma_scale_f32_16x16x128_f8f6f4 v[100:103], v[12:19], v[226:233], v[100:103], v219, v220 op_sel_hi:[0,0,0]
	s_setprio 0
	s_barrier
	s_add_i32 s42, s42, s57
	v_lshl_add_u64 v[182:183], s[52:53], 0, v[2:3]
	s_mov_b32 m0, s42
	ds_read_b128 v[196:199], v193 offset:16384
	ds_read_b128 v[204:207], v193 offset:18432
	ds_read_b128 v[200:203], v194 offset:16384
	ds_read_b128 v[208:211], v194 offset:18432
	ds_read_b128 v[226:229], v193 offset:20480
	ds_read_b128 v[234:237], v193 offset:22528
	ds_read_b128 v[230:233], v194 offset:20480
	ds_read_b128 v[238:241], v194 offset:22528
	global_load_lds_dwordx4 v[182:183], off
	s_add_i32 m0, s42, 0x2000
	s_add_u32 s70, s52, 0x40000
	v_lshl_add_u64 v[184:185], s[52:53], 0, v[164:165]
	s_addc_u32 s71, s53, 0
	s_add_i32 s42, s43, s57
	global_load_lds_dwordx4 v[184:185], off
	v_lshl_add_u64 v[174:175], s[70:71], 0, v[2:3]
	s_mov_b32 m0, s42
	v_lshl_add_u64 v[186:187], s[54:55], 0, v[168:169]
	global_load_lds_dwordx4 v[174:175], off
	v_lshl_add_u64 v[174:175], s[70:71], 0, v[164:165]
	s_add_i32 m0, s42, 0x2000
	v_lshl_add_u64 v[188:189], s[54:55], 0, v[166:167]
	global_load_lds_dwordx4 v[174:175], off
	s_mov_b32 m0, s47
	s_nop 0
	global_load_lds_dwordx4 v[186:187], off
	s_mov_b32 m0, s49
	s_nop 0
	global_load_lds_dwordx4 v[188:189], off
	s_waitcnt vmcnt(8)
	s_waitcnt lgkmcnt(0)
	s_barrier
	s_setprio 1
	s_waitcnt lgkmcnt(0)
	v_mfma_scale_f32_16x16x128_f8f6f4 v[96:99], v[20:27], v[196:203], v[96:99], v219, v220 op_sel_hi:[0,0,0]
	v_mfma_scale_f32_16x16x128_f8f6f4 v[88:91], v[28:35], v[196:203], v[88:91], v219, v220 op_sel_hi:[0,0,0]
	v_mfma_scale_f32_16x16x128_f8f6f4 v[80:83], v[20:27], v[204:211], v[80:83], v219, v220 op_sel_hi:[0,0,0]
	v_mfma_scale_f32_16x16x128_f8f6f4 v[72:75], v[28:35], v[204:211], v[72:75], v219, v220 op_sel_hi:[0,0,0]
	v_mfma_scale_f32_16x16x128_f8f6f4 v[64:67], v[20:27], v[226:233], v[64:67], v219, v220 op_sel_hi:[0,0,0]
	v_mfma_scale_f32_16x16x128_f8f6f4 v[56:59], v[28:35], v[226:233], v[56:59], v219, v220 op_sel_hi:[0,0,0]
	v_mfma_scale_f32_16x16x128_f8f6f4 v[48:51], v[20:27], v[234:241], v[48:51], v219, v220 op_sel_hi:[0,0,0]
	v_mfma_scale_f32_16x16x128_f8f6f4 v[40:43], v[28:35], v[234:241], v[40:43], v219, v220 op_sel_hi:[0,0,0]
	s_setprio 0
	s_setprio 1
	v_mfma_scale_f32_16x16x128_f8f6f4 v[92:95], v[4:11], v[196:203], v[92:95], v219, v220 op_sel_hi:[0,0,0]
	v_mfma_scale_f32_16x16x128_f8f6f4 v[84:87], v[12:19], v[196:203], v[84:87], v219, v220 op_sel_hi:[0,0,0]
	v_mfma_scale_f32_16x16x128_f8f6f4 v[76:79], v[4:11], v[204:211], v[76:79], v219, v220 op_sel_hi:[0,0,0]
	v_mfma_scale_f32_16x16x128_f8f6f4 v[68:71], v[12:19], v[204:211], v[68:71], v219, v220 op_sel_hi:[0,0,0]
	v_mfma_scale_f32_16x16x128_f8f6f4 v[60:63], v[4:11], v[226:233], v[60:63], v219, v220 op_sel_hi:[0,0,0]
	v_mfma_scale_f32_16x16x128_f8f6f4 v[52:55], v[12:19], v[226:233], v[52:55], v219, v220 op_sel_hi:[0,0,0]
	v_mfma_scale_f32_16x16x128_f8f6f4 v[44:47], v[4:11], v[234:241], v[44:47], v219, v220 op_sel_hi:[0,0,0]
	v_mfma_scale_f32_16x16x128_f8f6f4 v[36:39], v[12:19], v[234:241], v[36:39], v219, v220 op_sel_hi:[0,0,0]
	s_setprio 0
	s_barrier
	s_add_i32 s69, 0, 0x18000
	s_add_i32 s70, 0, 0x1c000
	ds_read_b128 v[4:7], v190 offset:32768
	ds_read_b128 v[12:15], v190 offset:34816
	ds_read_b128 v[8:11], v190 offset:33792
	ds_read_b128 v[16:19], v190 offset:35840
	ds_read_b128 v[20:23], v190 offset:49152
	ds_read_b128 v[28:31], v190 offset:51200
	ds_read_b128 v[24:27], v190 offset:50176
	ds_read_b128 v[32:35], v190 offset:52224
	s_add_u32 s42, s54, 0x40000
	s_addc_u32 s43, s55, 0
	s_mov_b32 m0, s61
	v_lshl_add_u64 v[174:175], s[42:43], 0, v[168:169]
	ds_read_b128 v[196:199], v193 offset:32768
	ds_read_b128 v[204:207], v193 offset:34816
	ds_read_b128 v[200:203], v194 offset:32768
	ds_read_b128 v[208:211], v194 offset:34816
	ds_read_b128 v[226:229], v193 offset:36864
	ds_read_b128 v[234:237], v193 offset:38912
	ds_read_b128 v[230:233], v194 offset:36864
	ds_read_b128 v[238:241], v194 offset:38912
	global_load_lds_dwordx4 v[174:175], off
	v_lshl_add_u64 v[174:175], s[42:43], 0, v[166:167]
	s_mov_b32 m0, s62
	s_nop 0
	global_load_lds_dwordx4 v[174:175], off
	s_waitcnt vmcnt(8)
	s_waitcnt lgkmcnt(0)
	s_barrier
	s_setprio 1
	s_waitcnt lgkmcnt(0)
	v_mfma_scale_f32_16x16x128_f8f6f4 v[160:163], v[4:11], v[196:203], v[160:163], v219, v220 op_sel_hi:[0,0,0]
	v_mfma_scale_f32_16x16x128_f8f6f4 v[152:155], v[12:19], v[196:203], v[152:155], v219, v220 op_sel_hi:[0,0,0]
	v_mfma_scale_f32_16x16x128_f8f6f4 v[144:147], v[4:11], v[204:211], v[144:147], v219, v220 op_sel_hi:[0,0,0]
	v_mfma_scale_f32_16x16x128_f8f6f4 v[136:139], v[12:19], v[204:211], v[136:139], v219, v220 op_sel_hi:[0,0,0]
	v_mfma_scale_f32_16x16x128_f8f6f4 v[128:131], v[4:11], v[226:233], v[128:131], v219, v220 op_sel_hi:[0,0,0]
	v_mfma_scale_f32_16x16x128_f8f6f4 v[120:123], v[12:19], v[226:233], v[120:123], v219, v220 op_sel_hi:[0,0,0]
	v_mfma_scale_f32_16x16x128_f8f6f4 v[112:115], v[4:11], v[234:241], v[112:115], v219, v220 op_sel_hi:[0,0,0]
	v_mfma_scale_f32_16x16x128_f8f6f4 v[104:107], v[12:19], v[234:241], v[104:107], v219, v220 op_sel_hi:[0,0,0]
	s_setprio 0
	s_setprio 1
	v_mfma_scale_f32_16x16x128_f8f6f4 v[156:159], v[20:27], v[196:203], v[156:159], v219, v220 op_sel_hi:[0,0,0]
	v_mfma_scale_f32_16x16x128_f8f6f4 v[148:151], v[28:35], v[196:203], v[148:151], v219, v220 op_sel_hi:[0,0,0]
	v_mfma_scale_f32_16x16x128_f8f6f4 v[140:143], v[20:27], v[204:211], v[140:143], v219, v220 op_sel_hi:[0,0,0]
	v_mfma_scale_f32_16x16x128_f8f6f4 v[132:135], v[28:35], v[204:211], v[132:135], v219, v220 op_sel_hi:[0,0,0]
	v_mfma_scale_f32_16x16x128_f8f6f4 v[124:127], v[20:27], v[226:233], v[124:127], v219, v220 op_sel_hi:[0,0,0]
	v_mfma_scale_f32_16x16x128_f8f6f4 v[116:119], v[28:35], v[226:233], v[116:119], v219, v220 op_sel_hi:[0,0,0]
	v_mfma_scale_f32_16x16x128_f8f6f4 v[108:111], v[20:27], v[234:241], v[108:111], v219, v220 op_sel_hi:[0,0,0]
	v_mfma_scale_f32_16x16x128_f8f6f4 v[100:103], v[28:35], v[234:241], v[100:103], v219, v220 op_sel_hi:[0,0,0]
	s_setprio 0
	s_barrier
	s_add_i32 s42, s69, s57
	v_lshl_add_u64 v[174:175], v[182:183], 0, s[6:7]
	s_mov_b32 m0, s42
	ds_read_b128 v[196:199], v193 offset:49152
	ds_read_b128 v[204:207], v193 offset:51200
	ds_read_b128 v[200:203], v194 offset:49152
	ds_read_b128 v[208:211], v194 offset:51200
	ds_read_b128 v[226:229], v193 offset:53248
	ds_read_b128 v[234:237], v193 offset:55296
	ds_read_b128 v[230:233], v194 offset:53248
	ds_read_b128 v[238:241], v194 offset:55296
	global_load_lds_dwordx4 v[174:175], off
	s_add_i32 m0, s42, 0x2000
	s_add_u32 s42, s52, 0x40080
	v_lshl_add_u64 v[174:175], v[184:185], 0, s[6:7]
	s_addc_u32 s43, s53, 0
	s_add_i32 s52, s70, s57
	global_load_lds_dwordx4 v[174:175], off
	v_lshl_add_u64 v[174:175], s[42:43], 0, v[2:3]
	s_mov_b32 m0, s52
	s_nop 0
	global_load_lds_dwordx4 v[174:175], off
	v_lshl_add_u64 v[174:175], s[42:43], 0, v[164:165]
	s_add_i32 m0, s52, 0x2000
	s_nop 0
	global_load_lds_dwordx4 v[174:175], off
	v_lshl_add_u64 v[174:175], v[186:187], 0, s[6:7]
	s_mov_b32 m0, s63
	s_nop 0
	global_load_lds_dwordx4 v[174:175], off
	v_lshl_add_u64 v[174:175], v[188:189], 0, s[6:7]
	s_mov_b32 m0, s64
	s_nop 0
	global_load_lds_dwordx4 v[174:175], off
	s_waitcnt vmcnt(8)
	s_waitcnt lgkmcnt(0)
	s_barrier
	s_setprio 1
	s_waitcnt lgkmcnt(0)
	v_mfma_scale_f32_16x16x128_f8f6f4 v[96:99], v[4:11], v[196:203], v[96:99], v219, v220 op_sel_hi:[0,0,0]
	v_mfma_scale_f32_16x16x128_f8f6f4 v[88:91], v[12:19], v[196:203], v[88:91], v219, v220 op_sel_hi:[0,0,0]
	v_mfma_scale_f32_16x16x128_f8f6f4 v[80:83], v[4:11], v[204:211], v[80:83], v219, v220 op_sel_hi:[0,0,0]
	v_mfma_scale_f32_16x16x128_f8f6f4 v[72:75], v[12:19], v[204:211], v[72:75], v219, v220 op_sel_hi:[0,0,0]
	v_mfma_scale_f32_16x16x128_f8f6f4 v[64:67], v[4:11], v[226:233], v[64:67], v219, v220 op_sel_hi:[0,0,0]
	v_mfma_scale_f32_16x16x128_f8f6f4 v[56:59], v[12:19], v[226:233], v[56:59], v219, v220 op_sel_hi:[0,0,0]
	v_mfma_scale_f32_16x16x128_f8f6f4 v[48:51], v[4:11], v[234:241], v[48:51], v219, v220 op_sel_hi:[0,0,0]
	v_mfma_scale_f32_16x16x128_f8f6f4 v[40:43], v[12:19], v[234:241], v[40:43], v219, v220 op_sel_hi:[0,0,0]
	s_setprio 0
	s_setprio 1
	v_mfma_scale_f32_16x16x128_f8f6f4 v[92:95], v[20:27], v[196:203], v[92:95], v219, v220 op_sel_hi:[0,0,0]
	v_mfma_scale_f32_16x16x128_f8f6f4 v[84:87], v[28:35], v[196:203], v[84:87], v219, v220 op_sel_hi:[0,0,0]
	v_mfma_scale_f32_16x16x128_f8f6f4 v[76:79], v[20:27], v[204:211], v[76:79], v219, v220 op_sel_hi:[0,0,0]
	v_mfma_scale_f32_16x16x128_f8f6f4 v[68:71], v[28:35], v[204:211], v[68:71], v219, v220 op_sel_hi:[0,0,0]
	v_mfma_scale_f32_16x16x128_f8f6f4 v[60:63], v[20:27], v[226:233], v[60:63], v219, v220 op_sel_hi:[0,0,0]
	v_mfma_scale_f32_16x16x128_f8f6f4 v[52:55], v[28:35], v[226:233], v[52:55], v219, v220 op_sel_hi:[0,0,0]
	v_mfma_scale_f32_16x16x128_f8f6f4 v[44:47], v[20:27], v[234:241], v[44:47], v219, v220 op_sel_hi:[0,0,0]
	v_mfma_scale_f32_16x16x128_f8f6f4 v[36:39], v[28:35], v[234:241], v[36:39], v219, v220 op_sel_hi:[0,0,0]
	s_setprio 0
	s_barrier
	s_add_i32 s68, s68, 2
	s_add_u32 s50, s50, 0x100
	s_addc_u32 s51, s51, 0
	s_add_u32 s66, s66, 0x100
	s_addc_u32 s67, s67, 0
	s_cmp_gt_u32 s68, 13
	s_cbranch_scc0 .LBB0_1772
	s_nop 15
	s_nop 15
	s_and_b64 vcc, exec, s[14:15]
	s_cbranch_vccz .LBB0_1775
	s_barrier

.LBB0_1802:
	v_lshrrev_b32_e32 v19, 4, v18
	v_and_b32_e32 v20, 15, v18
	v_lshl_or_b32 v1, s0, 6, v20
	v_bfe_u32 v19, v19, 1, 1
	s_lshl_b32 s0, s0, 13
	v_lshl_or_b32 v24, v19, 10, s0
	s_lshl_b32 s0, s1, 5
	s_and_b32 s11, s0, 0x60
	s_add_i32 m0, s49, 0x18000
	v_lshl_add_u64 v[10:11], v[10:11], 0, s[6:7]
	s_lshr_b32 s0, s11, 3
	s_waitcnt vmcnt(2)
	s_barrier
	global_load_lds_dwordx4 v[10:11], off
	v_lshl_add_u64 v[8:9], v[8:9], 0, s[6:7]
	s_add_i32 m0, s49, 0x1a000
	s_add_i32 s74, s49, 0x8000
	s_add_i32 s75, s49, 0xa000
	v_or_b32_e32 v19, s0, v19
	global_load_lds_dwordx4 v[8:9], off
	v_lshl_add_u64 v[4:5], v[4:5], 0, s[6:7]
	s_mov_b32 m0, s74
	s_add_u32 s0, s54, 0x40080
	global_load_lds_dwordx4 v[4:5], off
	v_lshl_add_u64 v[4:5], v[6:7], 0, s[6:7]
	s_mov_b32 m0, s75
	s_addc_u32 s1, s55, 0
	global_load_lds_dwordx4 v[4:5], off
	s_add_i32 m0, s49, 0x1c000
	v_lshl_add_u64 v[4:5], s[0:1], 0, v[2:3]
	global_load_lds_dwordx4 v[4:5], off
	v_lshl_add_u64 v[4:5], s[0:1], 0, v[168:169]
	s_add_i32 m0, s49, 0x1e000
	v_lshlrev_b32_e32 v22, 1, v18
	global_load_lds_dwordx4 v[4:5], off
	v_lshlrev_b32_e32 v4, 14, v12
	v_and_b32_e32 v4, 0xffff8000, v4
	v_lshl_add_u32 v4, v13, 11, v4
	v_and_b32_e32 v5, 1, v12
	v_lshl_or_b32 v4, v5, 6, v4
	v_bfe_u32 v21, v18, 4, 2
	v_and_b32_e32 v22, 32, v22
	v_lshlrev_b32_e32 v20, 6, v20
	v_lshlrev_b32_e32 v18, 2, v18
	v_lshl_add_u32 v170, v14, 1, v4
	v_lshlrev_b32_e32 v4, 14, v15
	v_or_b32_e32 v23, v20, v22
	v_and_b32_e32 v18, 32, v18
	v_and_b32_e32 v4, 0xffff8000, v4
	v_bitop3_b32 v20, v20, v18, v22 bitop3:0x36
	v_bitop3_b32 v25, v23, v18, 16 bitop3:0x36
	s_waitcnt vmcnt(6)
	v_lshl_add_u32 v4, v16, 11, v4
	v_and_b32_e32 v5, 1, v15
	v_or_b32_e32 v20, v20, v24
	v_or_b32_e32 v22, 16, v23
	v_or_b32_e32 v24, v25, v24
	v_lshlrev_b32_e32 v19, 10, v19
	s_cmpk_lt_u32 s10, 0x100
	v_lshl_or_b32 v4, v5, 6, v4
	v_bitop3_b32 v190, v19, v23, v18 bitop3:0xf6
	v_bitop3_b32 v191, v22, v19, v18 bitop3:0xde
	s_cselect_b64 s[36:37], -1, 0
	v_lshl_or_b32 v192, v21, 3, s11
	v_mov_b32_e32 v171, v3
	v_lshl_add_u32 v172, v17, 1, v4
	v_mov_b32_e32 v173, v3
	s_mov_b32 s76, 0
	v_add_u32_e32 v193, 0, v20
	v_add_u32_e32 v194, 0, v24
	v_and_b32_e32 v193, 15, v0
	v_lshlrev_b32_e32 v193, 6, v193
	v_bfe_u32 v194, v0, 4, 2
	v_lshl_or_b32 v193, v194, 4, v193
	v_and_b32_e32 v194, 8, v0
	v_lshlrev_b32_e32 v194, 2, v194
	v_xor_b32_e32 v193, v193, v194
	v_bfe_u32 v190, v0, 6, 2
	v_lshl_or_b32 v190, v190, 12, v193
	v_or_b32_e32 v191, 0x400, v190
	v_add_u32_e32 v190, 0x10000, v190
	v_lshrrev_b32_e32 v194, 8, v0
	v_lshl_or_b32 v193, v194, 13, v193
	v_or_b32_e32 v194, 0x400, v193
	s_barrier
	s_branch .LBB0_1805

.LBB0_1812:
	s_add_u32 s43, s52, 0xfffc0080
	s_addc_u32 s54, s53, -1
	s_add_i32 s42, 0, 0x10000
	s_cmp_eq_u32 s79, 12
	s_cselect_b32 s57, s10, s54
	s_cselect_b32 s56, s11, s43
	s_cselect_b32 s55, s39, s78
	s_cselect_b32 s54, s41, s77
	s_add_i32 s43, 0, 0x14000
	ds_read_b128 v[20:23], v190
	ds_read_b128 v[28:31], v190 offset:2048
	ds_read_b128 v[24:27], v190 offset:1024
	ds_read_b128 v[32:35], v190 offset:3072
	ds_read_b128 v[4:7], v190 offset:16384
	ds_read_b128 v[12:15], v190 offset:18432
	ds_read_b128 v[8:11], v190 offset:17408
	ds_read_b128 v[16:19], v190 offset:19456
	v_lshl_add_u64 v[174:175], s[52:53], 0, v[170:171]
	s_add_i32 m0, s49, 0xc000
	ds_read_b128 v[178:181], v193
	ds_read_b128 v[196:199], v193 offset:2048
	ds_read_b128 v[182:185], v194
	ds_read_b128 v[200:203], v194 offset:2048
	ds_read_b128 v[204:207], v193 offset:4096
	ds_read_b128 v[226:229], v193 offset:6144
	ds_read_b128 v[208:211], v194 offset:4096
	ds_read_b128 v[230:233], v194 offset:6144
	global_load_lds_dwordx4 v[174:175], off
	v_lshl_add_u64 v[174:175], s[52:53], 0, v[172:173]
	s_add_i32 m0, s49, 0xe000
	s_nop 0
	global_load_lds_dwordx4 v[174:175], off
	s_waitcnt vmcnt(8)
	s_waitcnt lgkmcnt(0)
	s_barrier
	s_setprio 1
	s_waitcnt lgkmcnt(0)
	v_mfma_scale_f32_16x16x128_f8f6f4 v[160:163], v[20:27], v[178:185], v[160:163], v219, v220 op_sel_hi:[0,0,0]
	v_mfma_scale_f32_16x16x128_f8f6f4 v[152:155], v[28:35], v[178:185], v[152:155], v219, v220 op_sel_hi:[0,0,0]
	v_mfma_scale_f32_16x16x128_f8f6f4 v[144:147], v[20:27], v[196:203], v[144:147], v219, v220 op_sel_hi:[0,0,0]
	v_mfma_scale_f32_16x16x128_f8f6f4 v[136:139], v[28:35], v[196:203], v[136:139], v219, v220 op_sel_hi:[0,0,0]
	v_mfma_scale_f32_16x16x128_f8f6f4 v[128:131], v[20:27], v[204:211], v[128:131], v219, v220 op_sel_hi:[0,0,0]
	v_mfma_scale_f32_16x16x128_f8f6f4 v[120:123], v[28:35], v[204:211], v[120:123], v219, v220 op_sel_hi:[0,0,0]
	v_mfma_scale_f32_16x16x128_f8f6f4 v[112:115], v[20:27], v[226:233], v[112:115], v219, v220 op_sel_hi:[0,0,0]
	v_mfma_scale_f32_16x16x128_f8f6f4 v[104:107], v[28:35], v[226:233], v[104:107], v219, v220 op_sel_hi:[0,0,0]
	s_setprio 0
	s_setprio 1
	v_mfma_scale_f32_16x16x128_f8f6f4 v[156:159], v[4:11], v[178:185], v[156:159], v219, v220 op_sel_hi:[0,0,0]
	v_mfma_scale_f32_16x16x128_f8f6f4 v[148:151], v[12:19], v[178:185], v[148:151], v219, v220 op_sel_hi:[0,0,0]
	v_mfma_scale_f32_16x16x128_f8f6f4 v[140:143], v[4:11], v[196:203], v[140:143], v219, v220 op_sel_hi:[0,0,0]
	v_mfma_scale_f32_16x16x128_f8f6f4 v[132:135], v[12:19], v[196:203], v[132:135], v219, v220 op_sel_hi:[0,0,0]
	v_mfma_scale_f32_16x16x128_f8f6f4 v[124:127], v[4:11], v[204:211], v[124:127], v219, v220 op_sel_hi:[0,0,0]
	v_mfma_scale_f32_16x16x128_f8f6f4 v[116:119], v[12:19], v[204:211], v[116:119], v219, v220 op_sel_hi:[0,0,0]
	v_mfma_scale_f32_16x16x128_f8f6f4 v[108:111], v[4:11], v[226:233], v[108:111], v219, v220 op_sel_hi:[0,0,0]
	v_mfma_scale_f32_16x16x128_f8f6f4 v[100:103], v[12:19], v[226:233], v[100:103], v219, v220 op_sel_hi:[0,0,0]
	s_setprio 0
	s_barrier
	s_add_i32 s42, s42, s69
	v_lshl_add_u64 v[182:183], s[54:55], 0, v[2:3]
	s_mov_b32 m0, s42
	ds_read_b128 v[196:199], v193 offset:16384
	ds_read_b128 v[204:207], v193 offset:18432
	ds_read_b128 v[200:203], v194 offset:16384
	ds_read_b128 v[208:211], v194 offset:18432
	ds_read_b128 v[226:229], v193 offset:20480
	ds_read_b128 v[234:237], v193 offset:22528
	ds_read_b128 v[230:233], v194 offset:20480
	ds_read_b128 v[238:241], v194 offset:22528
	global_load_lds_dwordx4 v[182:183], off
	s_add_i32 m0, s42, 0x2000
	s_add_u32 s80, s54, 0x40000
	v_lshl_add_u64 v[184:185], s[54:55], 0, v[168:169]
	s_addc_u32 s81, s55, 0
	s_add_i32 s42, s43, s69
	global_load_lds_dwordx4 v[184:185], off
	v_lshl_add_u64 v[174:175], s[80:81], 0, v[2:3]
	s_mov_b32 m0, s42
	v_lshl_add_u64 v[186:187], s[56:57], 0, v[164:165]
	global_load_lds_dwordx4 v[174:175], off
	v_lshl_add_u64 v[174:175], s[80:81], 0, v[168:169]
	s_add_i32 m0, s42, 0x2000
	v_lshl_add_u64 v[188:189], s[56:57], 0, v[166:167]
	global_load_lds_dwordx4 v[174:175], off
	s_mov_b32 m0, s49
	s_nop 0
	global_load_lds_dwordx4 v[186:187], off
	s_mov_b32 m0, s51
	s_nop 0
	global_load_lds_dwordx4 v[188:189], off
	s_waitcnt vmcnt(8)
	s_waitcnt lgkmcnt(0)
	s_barrier
	s_setprio 1
	s_waitcnt lgkmcnt(0)
	v_mfma_scale_f32_16x16x128_f8f6f4 v[96:99], v[20:27], v[196:203], v[96:99], v219, v220 op_sel_hi:[0,0,0]
	v_mfma_scale_f32_16x16x128_f8f6f4 v[88:91], v[28:35], v[196:203], v[88:91], v219, v220 op_sel_hi:[0,0,0]
	v_mfma_scale_f32_16x16x128_f8f6f4 v[80:83], v[20:27], v[204:211], v[80:83], v219, v220 op_sel_hi:[0,0,0]
	v_mfma_scale_f32_16x16x128_f8f6f4 v[72:75], v[28:35], v[204:211], v[72:75], v219, v220 op_sel_hi:[0,0,0]
	v_mfma_scale_f32_16x16x128_f8f6f4 v[64:67], v[20:27], v[226:233], v[64:67], v219, v220 op_sel_hi:[0,0,0]
	v_mfma_scale_f32_16x16x128_f8f6f4 v[56:59], v[28:35], v[226:233], v[56:59], v219, v220 op_sel_hi:[0,0,0]
	v_mfma_scale_f32_16x16x128_f8f6f4 v[48:51], v[20:27], v[234:241], v[48:51], v219, v220 op_sel_hi:[0,0,0]
	v_mfma_scale_f32_16x16x128_f8f6f4 v[40:43], v[28:35], v[234:241], v[40:43], v219, v220 op_sel_hi:[0,0,0]
	s_setprio 0
	s_setprio 1
	v_mfma_scale_f32_16x16x128_f8f6f4 v[92:95], v[4:11], v[196:203], v[92:95], v219, v220 op_sel_hi:[0,0,0]
	v_mfma_scale_f32_16x16x128_f8f6f4 v[84:87], v[12:19], v[196:203], v[84:87], v219, v220 op_sel_hi:[0,0,0]
	v_mfma_scale_f32_16x16x128_f8f6f4 v[76:79], v[4:11], v[204:211], v[76:79], v219, v220 op_sel_hi:[0,0,0]
	v_mfma_scale_f32_16x16x128_f8f6f4 v[68:71], v[12:19], v[204:211], v[68:71], v219, v220 op_sel_hi:[0,0,0]
	v_mfma_scale_f32_16x16x128_f8f6f4 v[60:63], v[4:11], v[226:233], v[60:63], v219, v220 op_sel_hi:[0,0,0]
	v_mfma_scale_f32_16x16x128_f8f6f4 v[52:55], v[12:19], v[226:233], v[52:55], v219, v220 op_sel_hi:[0,0,0]
	v_mfma_scale_f32_16x16x128_f8f6f4 v[44:47], v[4:11], v[234:241], v[44:47], v219, v220 op_sel_hi:[0,0,0]
	v_mfma_scale_f32_16x16x128_f8f6f4 v[36:39], v[12:19], v[234:241], v[36:39], v219, v220 op_sel_hi:[0,0,0]
	s_setprio 0
	s_barrier
	s_add_i32 s80, 0, 0x18000
	s_add_i32 s81, 0, 0x1c000
	ds_read_b128 v[4:7], v190 offset:32768
	ds_read_b128 v[12:15], v190 offset:34816
	ds_read_b128 v[8:11], v190 offset:33792
	ds_read_b128 v[16:19], v190 offset:35840
	ds_read_b128 v[20:23], v190 offset:49152
	ds_read_b128 v[28:31], v190 offset:51200
	ds_read_b128 v[24:27], v190 offset:50176
	ds_read_b128 v[32:35], v190 offset:52224
	s_add_u32 s42, s56, 0x40000
	s_addc_u32 s43, s57, 0
	s_mov_b32 m0, s72
	v_lshl_add_u64 v[174:175], s[42:43], 0, v[164:165]
	ds_read_b128 v[196:199], v193 offset:32768
	ds_read_b128 v[204:207], v193 offset:34816
	ds_read_b128 v[200:203], v194 offset:32768
	ds_read_b128 v[208:211], v194 offset:34816
	ds_read_b128 v[226:229], v193 offset:36864
	ds_read_b128 v[234:237], v193 offset:38912
	ds_read_b128 v[230:233], v194 offset:36864
	ds_read_b128 v[238:241], v194 offset:38912
	global_load_lds_dwordx4 v[174:175], off
	v_lshl_add_u64 v[174:175], s[42:43], 0, v[166:167]
	s_mov_b32 m0, s73
	s_nop 0
	global_load_lds_dwordx4 v[174:175], off
	s_waitcnt vmcnt(8)
	s_waitcnt lgkmcnt(0)
	s_barrier
	s_setprio 1
	s_waitcnt lgkmcnt(0)
	v_mfma_scale_f32_16x16x128_f8f6f4 v[160:163], v[4:11], v[196:203], v[160:163], v219, v220 op_sel_hi:[0,0,0]
	v_mfma_scale_f32_16x16x128_f8f6f4 v[152:155], v[12:19], v[196:203], v[152:155], v219, v220 op_sel_hi:[0,0,0]
	v_mfma_scale_f32_16x16x128_f8f6f4 v[144:147], v[4:11], v[204:211], v[144:147], v219, v220 op_sel_hi:[0,0,0]
	v_mfma_scale_f32_16x16x128_f8f6f4 v[136:139], v[12:19], v[204:211], v[136:139], v219, v220 op_sel_hi:[0,0,0]
	v_mfma_scale_f32_16x16x128_f8f6f4 v[128:131], v[4:11], v[226:233], v[128:131], v219, v220 op_sel_hi:[0,0,0]
	v_mfma_scale_f32_16x16x128_f8f6f4 v[120:123], v[12:19], v[226:233], v[120:123], v219, v220 op_sel_hi:[0,0,0]
	v_mfma_scale_f32_16x16x128_f8f6f4 v[112:115], v[4:11], v[234:241], v[112:115], v219, v220 op_sel_hi:[0,0,0]
	v_mfma_scale_f32_16x16x128_f8f6f4 v[104:107], v[12:19], v[234:241], v[104:107], v219, v220 op_sel_hi:[0,0,0]
	s_setprio 0
	s_setprio 1
	v_mfma_scale_f32_16x16x128_f8f6f4 v[156:159], v[20:27], v[196:203], v[156:159], v219, v220 op_sel_hi:[0,0,0]
	v_mfma_scale_f32_16x16x128_f8f6f4 v[148:151], v[28:35], v[196:203], v[148:151], v219, v220 op_sel_hi:[0,0,0]
	v_mfma_scale_f32_16x16x128_f8f6f4 v[140:143], v[20:27], v[204:211], v[140:143], v219, v220 op_sel_hi:[0,0,0]
	v_mfma_scale_f32_16x16x128_f8f6f4 v[132:135], v[28:35], v[204:211], v[132:135], v219, v220 op_sel_hi:[0,0,0]
	v_mfma_scale_f32_16x16x128_f8f6f4 v[124:127], v[20:27], v[226:233], v[124:127], v219, v220 op_sel_hi:[0,0,0]
	v_mfma_scale_f32_16x16x128_f8f6f4 v[116:119], v[28:35], v[226:233], v[116:119], v219, v220 op_sel_hi:[0,0,0]
	v_mfma_scale_f32_16x16x128_f8f6f4 v[108:111], v[20:27], v[234:241], v[108:111], v219, v220 op_sel_hi:[0,0,0]
	v_mfma_scale_f32_16x16x128_f8f6f4 v[100:103], v[28:35], v[234:241], v[100:103], v219, v220 op_sel_hi:[0,0,0]
	s_setprio 0
	s_barrier
	s_add_i32 s42, s80, s69
	v_lshl_add_u64 v[174:175], v[182:183], 0, s[6:7]
	s_mov_b32 m0, s42
	ds_read_b128 v[196:199], v193 offset:49152
	ds_read_b128 v[204:207], v193 offset:51200
	ds_read_b128 v[200:203], v194 offset:49152
	ds_read_b128 v[208:211], v194 offset:51200
	ds_read_b128 v[226:229], v193 offset:53248
	ds_read_b128 v[234:237], v193 offset:55296
	ds_read_b128 v[230:233], v194 offset:53248
	ds_read_b128 v[238:241], v194 offset:55296
	global_load_lds_dwordx4 v[174:175], off
	s_add_i32 m0, s42, 0x2000
	s_add_u32 s42, s54, 0x40080
	v_lshl_add_u64 v[174:175], v[184:185], 0, s[6:7]
	s_addc_u32 s43, s55, 0
	s_add_i32 s54, s81, s69
	global_load_lds_dwordx4 v[174:175], off
	v_lshl_add_u64 v[174:175], s[42:43], 0, v[2:3]
	s_mov_b32 m0, s54
	s_nop 0
	global_load_lds_dwordx4 v[174:175], off
	v_lshl_add_u64 v[174:175], s[42:43], 0, v[168:169]
	s_add_i32 m0, s54, 0x2000
	s_nop 0
	global_load_lds_dwordx4 v[174:175], off
	v_lshl_add_u64 v[174:175], v[186:187], 0, s[6:7]
	s_mov_b32 m0, s74
	s_nop 0
	global_load_lds_dwordx4 v[174:175], off
	v_lshl_add_u64 v[174:175], v[188:189], 0, s[6:7]
	s_mov_b32 m0, s75
	s_nop 0
	global_load_lds_dwordx4 v[174:175], off
	s_waitcnt vmcnt(8)
	s_waitcnt lgkmcnt(0)
	s_barrier
	s_setprio 1
	s_waitcnt lgkmcnt(0)
	v_mfma_scale_f32_16x16x128_f8f6f4 v[96:99], v[4:11], v[196:203], v[96:99], v219, v220 op_sel_hi:[0,0,0]
	v_mfma_scale_f32_16x16x128_f8f6f4 v[88:91], v[12:19], v[196:203], v[88:91], v219, v220 op_sel_hi:[0,0,0]
	v_mfma_scale_f32_16x16x128_f8f6f4 v[80:83], v[4:11], v[204:211], v[80:83], v219, v220 op_sel_hi:[0,0,0]
	v_mfma_scale_f32_16x16x128_f8f6f4 v[72:75], v[12:19], v[204:211], v[72:75], v219, v220 op_sel_hi:[0,0,0]
	v_mfma_scale_f32_16x16x128_f8f6f4 v[64:67], v[4:11], v[226:233], v[64:67], v219, v220 op_sel_hi:[0,0,0]
	v_mfma_scale_f32_16x16x128_f8f6f4 v[56:59], v[12:19], v[226:233], v[56:59], v219, v220 op_sel_hi:[0,0,0]
	v_mfma_scale_f32_16x16x128_f8f6f4 v[48:51], v[4:11], v[234:241], v[48:51], v219, v220 op_sel_hi:[0,0,0]
	v_mfma_scale_f32_16x16x128_f8f6f4 v[40:43], v[12:19], v[234:241], v[40:43], v219, v220 op_sel_hi:[0,0,0]
	s_setprio 0
	s_setprio 1
	v_mfma_scale_f32_16x16x128_f8f6f4 v[92:95], v[20:27], v[196:203], v[92:95], v219, v220 op_sel_hi:[0,0,0]
	v_mfma_scale_f32_16x16x128_f8f6f4 v[84:87], v[28:35], v[196:203], v[84:87], v219, v220 op_sel_hi:[0,0,0]
	v_mfma_scale_f32_16x16x128_f8f6f4 v[76:79], v[20:27], v[204:211], v[76:79], v219, v220 op_sel_hi:[0,0,0]
	v_mfma_scale_f32_16x16x128_f8f6f4 v[68:71], v[28:35], v[204:211], v[68:71], v219, v220 op_sel_hi:[0,0,0]
	v_mfma_scale_f32_16x16x128_f8f6f4 v[60:63], v[20:27], v[226:233], v[60:63], v219, v220 op_sel_hi:[0,0,0]
	v_mfma_scale_f32_16x16x128_f8f6f4 v[52:55], v[28:35], v[226:233], v[52:55], v219, v220 op_sel_hi:[0,0,0]
	v_mfma_scale_f32_16x16x128_f8f6f4 v[44:47], v[20:27], v[234:241], v[44:47], v219, v220 op_sel_hi:[0,0,0]
	v_mfma_scale_f32_16x16x128_f8f6f4 v[36:39], v[28:35], v[234:241], v[36:39], v219, v220 op_sel_hi:[0,0,0]
	s_setprio 0
	s_barrier
	s_add_i32 s79, s79, 2
	s_add_u32 s52, s52, 0x100
	s_addc_u32 s53, s53, 0
	s_add_u32 s77, s77, 0x100
	s_addc_u32 s78, s78, 0
	s_cmp_gt_u32 s79, 13
	s_cbranch_scc0 .LBB0_1812
	s_nop 15
	s_nop 15
	s_and_b64 vcc, exec, s[36:37]
	v_readlane_b32 s78, v249, 36
	s_mov_b32 s79, s28
	s_cbranch_vccz .LBB0_1815
	s_barrier

.LBB0_1880:
	v_readlane_b32 s40, v254, 24
	v_lshrrev_b32_e32 v15, 4, v14
	v_and_b32_e32 v20, 15, v14
	s_lshl_b32 s1, s1, 5
	v_mov_b32_e32 v169, v3
	v_readlane_b32 s41, v254, 25
	v_lshl_or_b32 v1, s4, 6, v20
	v_bfe_u32 v15, v15, 1, 1
	s_lshl_b32 s4, s4, 13
	s_and_b32 s1, s1, 0x60
	s_add_i32 m0, s11, 0x18000
	v_lshl_add_u64 v[4:5], v[4:5], 0, s[6:7]
	v_lshl_add_u64 v[16:17], s[40:41], 0, v[168:169]
	v_mov_b32_e32 v167, v3
	v_lshl_or_b32 v24, v15, 10, s4
	s_lshr_b32 s4, s1, 3
	s_waitcnt vmcnt(2)
	s_barrier
	global_load_lds_dwordx4 v[4:5], off
	v_lshl_add_u64 v[4:5], v[6:7], 0, s[6:7]
	s_add_i32 m0, s11, 0x1a000
	s_add_i32 s52, s11, 0x8000
	s_add_i32 s53, s11, 0xa000
	v_lshl_add_u64 v[18:19], s[40:41], 0, v[166:167]
	v_or_b32_e32 v15, s4, v15
	global_load_lds_dwordx4 v[4:5], off
	v_lshl_add_u64 v[4:5], v[16:17], 0, s[6:7]
	s_mov_b32 m0, s52
	s_add_u32 s4, s44, 0xb0080
	global_load_lds_dwordx4 v[4:5], off
	v_lshl_add_u64 v[4:5], v[18:19], 0, s[6:7]
	s_mov_b32 m0, s53
	s_addc_u32 s5, s45, 0
	global_load_lds_dwordx4 v[4:5], off
	s_add_i32 m0, s11, 0x1c000
	v_lshl_add_u64 v[4:5], s[4:5], 0, v[2:3]
	global_load_lds_dwordx4 v[4:5], off
	v_lshl_add_u64 v[4:5], s[4:5], 0, v[164:165]
	s_add_i32 m0, s11, 0x1e000
	s_movk_i32 s5, 0x1600
	global_load_lds_dwordx4 v[4:5], off
	v_bfe_u32 v21, v14, 4, 2
	v_lshrrev_b32_e32 v5, 1, v12
	v_mul_lo_u32 v4, v11, s5
	s_mov_b32 s4, 0x16000
	s_cmpk_lt_u32 s0, 0x100
	v_lshl_or_b32 v192, v21, 3, s1
	v_mad_u64_u32 v[4:5], s[0:1], v5, s4, v[4:5]
	v_and_b32_e32 v5, 1, v12
	v_lshlrev_b32_e32 v22, 1, v14
	v_lshl_or_b32 v4, v5, 6, v4
	v_and_b32_e32 v22, 32, v22
	v_lshlrev_b32_e32 v20, 6, v20
	v_lshlrev_b32_e32 v14, 2, v14
	v_lshl_add_u32 v170, v13, 1, v4
	v_lshrrev_b32_e32 v5, 1, v8
	v_mul_lo_u32 v4, v9, s5
	v_or_b32_e32 v23, v20, v22
	v_and_b32_e32 v14, 32, v14
	v_mad_u64_u32 v[4:5], s[0:1], v5, s4, v[4:5]
	v_bitop3_b32 v20, v20, v14, v22 bitop3:0x36
	v_bitop3_b32 v25, v23, v14, 16 bitop3:0x36
	s_waitcnt vmcnt(6)
	v_and_b32_e32 v5, 1, v8
	v_or_b32_e32 v20, v20, v24
	v_or_b32_e32 v22, 16, v23
	v_or_b32_e32 v24, v25, v24
	v_lshlrev_b32_e32 v15, 10, v15
	v_lshl_or_b32 v4, v5, 6, v4
	v_readlane_b32 s0, v254, 20
	v_bitop3_b32 v190, v15, v23, v14 bitop3:0xf6
	v_bitop3_b32 v191, v22, v15, v14 bitop3:0xde
	s_cselect_b64 s[36:37], -1, 0
	v_mov_b32_e32 v171, v3
	v_lshl_add_u32 v172, v10, 1, v4
	v_mov_b32_e32 v173, v3
	s_mov_b32 s54, 0
	v_add_u32_e32 v193, 0, v20
	v_add_u32_e32 v194, 0, v24
	v_and_b32_e32 v193, 15, v0
	v_lshlrev_b32_e32 v193, 6, v193
	v_bfe_u32 v194, v0, 4, 2
	v_lshl_or_b32 v193, v194, 4, v193
	v_and_b32_e32 v194, 8, v0
	v_lshlrev_b32_e32 v194, 2, v194
	v_xor_b32_e32 v193, v193, v194
	v_bfe_u32 v190, v0, 6, 2
	v_lshl_or_b32 v190, v190, 12, v193
	v_or_b32_e32 v191, 0x400, v190
	v_add_u32_e32 v190, 0x10000, v190
	v_lshrrev_b32_e32 v194, 8, v0
	v_lshl_or_b32 v193, v194, 13, v193
	v_or_b32_e32 v194, 0x400, v193
	v_readlane_b32 s57, v254, 9
	s_mov_b32 s58, s0
	s_barrier
	v_readlane_b32 s1, v254, 21
	s_branch .LBB0_1883

.LBB0_1894:
	s_add_u32 s43, s40, 0xfff50080
	s_addc_u32 s44, s41, -1
	s_add_i32 s42, 0, 0x10000
	s_cmp_eq_u32 s61, 40
	s_cselect_b32 s47, s5, s44
	s_cselect_b32 s46, s4, s43
	s_cselect_b32 s45, s39, s60
	s_cselect_b32 s44, s38, s59
	s_add_i32 s43, 0, 0x14000
	ds_read_b128 v[20:23], v190
	ds_read_b128 v[28:31], v190 offset:2048
	ds_read_b128 v[24:27], v190 offset:1024
	ds_read_b128 v[32:35], v190 offset:3072
	ds_read_b128 v[4:7], v190 offset:16384
	ds_read_b128 v[12:15], v190 offset:18432
	ds_read_b128 v[8:11], v190 offset:17408
	ds_read_b128 v[16:19], v190 offset:19456
	v_lshl_add_u64 v[174:175], s[40:41], 0, v[170:171]
	s_add_i32 m0, s11, 0xc000
	ds_read_b128 v[178:181], v193
	ds_read_b128 v[196:199], v193 offset:2048
	ds_read_b128 v[182:185], v194
	ds_read_b128 v[200:203], v194 offset:2048
	ds_read_b128 v[204:207], v193 offset:4096
	ds_read_b128 v[226:229], v193 offset:6144
	ds_read_b128 v[208:211], v194 offset:4096
	ds_read_b128 v[230:233], v194 offset:6144
	global_load_lds_dwordx4 v[174:175], off
	v_lshl_add_u64 v[174:175], s[40:41], 0, v[172:173]
	s_add_i32 m0, s11, 0xe000
	s_nop 0
	global_load_lds_dwordx4 v[174:175], off
	s_waitcnt vmcnt(8)
	s_waitcnt lgkmcnt(0)
	s_barrier
	s_setprio 1
	s_waitcnt lgkmcnt(0)
	v_mfma_scale_f32_16x16x128_f8f6f4 v[160:163], v[20:27], v[178:185], v[160:163], v219, v220 op_sel_hi:[0,0,0]
	v_mfma_scale_f32_16x16x128_f8f6f4 v[156:159], v[28:35], v[178:185], v[156:159], v219, v220 op_sel_hi:[0,0,0]
	v_mfma_scale_f32_16x16x128_f8f6f4 v[152:155], v[20:27], v[196:203], v[152:155], v219, v220 op_sel_hi:[0,0,0]
	v_mfma_scale_f32_16x16x128_f8f6f4 v[148:151], v[28:35], v[196:203], v[148:151], v219, v220 op_sel_hi:[0,0,0]
	v_mfma_scale_f32_16x16x128_f8f6f4 v[136:139], v[20:27], v[204:211], v[136:139], v219, v220 op_sel_hi:[0,0,0]
	v_mfma_scale_f32_16x16x128_f8f6f4 v[132:135], v[28:35], v[204:211], v[132:135], v219, v220 op_sel_hi:[0,0,0]
	v_mfma_scale_f32_16x16x128_f8f6f4 v[120:123], v[20:27], v[226:233], v[120:123], v219, v220 op_sel_hi:[0,0,0]
	v_mfma_scale_f32_16x16x128_f8f6f4 v[116:119], v[28:35], v[226:233], v[116:119], v219, v220 op_sel_hi:[0,0,0]
	s_setprio 0
	s_setprio 1
	v_mfma_scale_f32_16x16x128_f8f6f4 v[144:147], v[4:11], v[178:185], v[144:147], v219, v220 op_sel_hi:[0,0,0]
	v_mfma_scale_f32_16x16x128_f8f6f4 v[140:143], v[12:19], v[178:185], v[140:143], v219, v220 op_sel_hi:[0,0,0]
	v_mfma_scale_f32_16x16x128_f8f6f4 v[128:131], v[4:11], v[196:203], v[128:131], v219, v220 op_sel_hi:[0,0,0]
	v_mfma_scale_f32_16x16x128_f8f6f4 v[124:127], v[12:19], v[196:203], v[124:127], v219, v220 op_sel_hi:[0,0,0]
	v_mfma_scale_f32_16x16x128_f8f6f4 v[112:115], v[4:11], v[204:211], v[112:115], v219, v220 op_sel_hi:[0,0,0]
	v_mfma_scale_f32_16x16x128_f8f6f4 v[108:111], v[12:19], v[204:211], v[108:111], v219, v220 op_sel_hi:[0,0,0]
	v_mfma_scale_f32_16x16x128_f8f6f4 v[104:107], v[4:11], v[226:233], v[104:107], v219, v220 op_sel_hi:[0,0,0]
	v_mfma_scale_f32_16x16x128_f8f6f4 v[100:103], v[12:19], v[226:233], v[100:103], v219, v220 op_sel_hi:[0,0,0]
	s_setprio 0
	s_barrier
	s_add_i32 s42, s42, s10
	v_lshl_add_u64 v[182:183], s[44:45], 0, v[2:3]
	s_mov_b32 m0, s42
	ds_read_b128 v[196:199], v193 offset:16384
	ds_read_b128 v[204:207], v193 offset:18432
	ds_read_b128 v[200:203], v194 offset:16384
	ds_read_b128 v[208:211], v194 offset:18432
	ds_read_b128 v[226:229], v193 offset:20480
	ds_read_b128 v[234:237], v193 offset:22528
	ds_read_b128 v[230:233], v194 offset:20480
	ds_read_b128 v[238:241], v194 offset:22528
	global_load_lds_dwordx4 v[182:183], off
	s_add_i32 m0, s42, 0x2000
	s_add_u32 s62, s44, 0xb0000
	v_lshl_add_u64 v[184:185], s[44:45], 0, v[164:165]
	s_addc_u32 s63, s45, 0
	s_add_i32 s42, s43, s10
	global_load_lds_dwordx4 v[184:185], off
	v_lshl_add_u64 v[174:175], s[62:63], 0, v[2:3]
	s_mov_b32 m0, s42
	v_lshl_add_u64 v[186:187], s[46:47], 0, v[168:169]
	global_load_lds_dwordx4 v[174:175], off
	v_lshl_add_u64 v[174:175], s[62:63], 0, v[164:165]
	s_add_i32 m0, s42, 0x2000
	v_lshl_add_u64 v[188:189], s[46:47], 0, v[166:167]
	global_load_lds_dwordx4 v[174:175], off
	s_mov_b32 m0, s11
	s_nop 0
	global_load_lds_dwordx4 v[186:187], off
	s_mov_b32 m0, s12
	s_nop 0
	global_load_lds_dwordx4 v[188:189], off
	s_waitcnt vmcnt(8)
	s_waitcnt lgkmcnt(0)
	s_barrier
	s_setprio 1
	s_waitcnt lgkmcnt(0)
	v_mfma_scale_f32_16x16x128_f8f6f4 v[96:99], v[20:27], v[196:203], v[96:99], v219, v220 op_sel_hi:[0,0,0]
	v_mfma_scale_f32_16x16x128_f8f6f4 v[92:95], v[28:35], v[196:203], v[92:95], v219, v220 op_sel_hi:[0,0,0]
	v_mfma_scale_f32_16x16x128_f8f6f4 v[88:91], v[20:27], v[204:211], v[88:91], v219, v220 op_sel_hi:[0,0,0]
	v_mfma_scale_f32_16x16x128_f8f6f4 v[84:87], v[28:35], v[204:211], v[84:87], v219, v220 op_sel_hi:[0,0,0]
	v_mfma_scale_f32_16x16x128_f8f6f4 v[72:75], v[20:27], v[226:233], v[72:75], v219, v220 op_sel_hi:[0,0,0]
	v_mfma_scale_f32_16x16x128_f8f6f4 v[68:71], v[28:35], v[226:233], v[68:71], v219, v220 op_sel_hi:[0,0,0]
	v_mfma_scale_f32_16x16x128_f8f6f4 v[56:59], v[20:27], v[234:241], v[56:59], v219, v220 op_sel_hi:[0,0,0]
	v_mfma_scale_f32_16x16x128_f8f6f4 v[52:55], v[28:35], v[234:241], v[52:55], v219, v220 op_sel_hi:[0,0,0]
	s_setprio 0
	s_setprio 1
	v_mfma_scale_f32_16x16x128_f8f6f4 v[80:83], v[4:11], v[196:203], v[80:83], v219, v220 op_sel_hi:[0,0,0]
	v_mfma_scale_f32_16x16x128_f8f6f4 v[76:79], v[12:19], v[196:203], v[76:79], v219, v220 op_sel_hi:[0,0,0]
	v_mfma_scale_f32_16x16x128_f8f6f4 v[64:67], v[4:11], v[204:211], v[64:67], v219, v220 op_sel_hi:[0,0,0]
	v_mfma_scale_f32_16x16x128_f8f6f4 v[60:63], v[12:19], v[204:211], v[60:63], v219, v220 op_sel_hi:[0,0,0]
	v_mfma_scale_f32_16x16x128_f8f6f4 v[48:51], v[4:11], v[226:233], v[48:51], v219, v220 op_sel_hi:[0,0,0]
	v_mfma_scale_f32_16x16x128_f8f6f4 v[44:47], v[12:19], v[226:233], v[44:47], v219, v220 op_sel_hi:[0,0,0]
	v_mfma_scale_f32_16x16x128_f8f6f4 v[40:43], v[4:11], v[234:241], v[40:43], v219, v220 op_sel_hi:[0,0,0]
	v_mfma_scale_f32_16x16x128_f8f6f4 v[36:39], v[12:19], v[234:241], v[36:39], v219, v220 op_sel_hi:[0,0,0]
	s_setprio 0
	s_barrier
	s_add_i32 s62, 0, 0x18000
	s_add_i32 s63, 0, 0x1c000
	ds_read_b128 v[4:7], v190 offset:32768
	ds_read_b128 v[12:15], v190 offset:34816
	ds_read_b128 v[8:11], v190 offset:33792
	ds_read_b128 v[16:19], v190 offset:35840
	ds_read_b128 v[20:23], v190 offset:49152
	ds_read_b128 v[28:31], v190 offset:51200
	ds_read_b128 v[24:27], v190 offset:50176
	ds_read_b128 v[32:35], v190 offset:52224
	s_add_u32 s42, s46, 0xb0000
	s_addc_u32 s43, s47, 0
	s_mov_b32 m0, s48
	v_lshl_add_u64 v[174:175], s[42:43], 0, v[168:169]
	ds_read_b128 v[196:199], v193 offset:32768
	ds_read_b128 v[204:207], v193 offset:34816
	ds_read_b128 v[200:203], v194 offset:32768
	ds_read_b128 v[208:211], v194 offset:34816
	ds_read_b128 v[226:229], v193 offset:36864
	ds_read_b128 v[234:237], v193 offset:38912
	ds_read_b128 v[230:233], v194 offset:36864
	ds_read_b128 v[238:241], v194 offset:38912
	global_load_lds_dwordx4 v[174:175], off
	v_lshl_add_u64 v[174:175], s[42:43], 0, v[166:167]
	s_mov_b32 m0, s49
	s_nop 0
	global_load_lds_dwordx4 v[174:175], off
	s_waitcnt vmcnt(8)
	s_waitcnt lgkmcnt(0)
	s_barrier
	s_setprio 1
	s_waitcnt lgkmcnt(0)
	v_mfma_scale_f32_16x16x128_f8f6f4 v[160:163], v[4:11], v[196:203], v[160:163], v219, v220 op_sel_hi:[0,0,0]
	v_mfma_scale_f32_16x16x128_f8f6f4 v[156:159], v[12:19], v[196:203], v[156:159], v219, v220 op_sel_hi:[0,0,0]
	v_mfma_scale_f32_16x16x128_f8f6f4 v[152:155], v[4:11], v[204:211], v[152:155], v219, v220 op_sel_hi:[0,0,0]
	v_mfma_scale_f32_16x16x128_f8f6f4 v[148:151], v[12:19], v[204:211], v[148:151], v219, v220 op_sel_hi:[0,0,0]
	v_mfma_scale_f32_16x16x128_f8f6f4 v[136:139], v[4:11], v[226:233], v[136:139], v219, v220 op_sel_hi:[0,0,0]
	v_mfma_scale_f32_16x16x128_f8f6f4 v[132:135], v[12:19], v[226:233], v[132:135], v219, v220 op_sel_hi:[0,0,0]
	v_mfma_scale_f32_16x16x128_f8f6f4 v[120:123], v[4:11], v[234:241], v[120:123], v219, v220 op_sel_hi:[0,0,0]
	v_mfma_scale_f32_16x16x128_f8f6f4 v[116:119], v[12:19], v[234:241], v[116:119], v219, v220 op_sel_hi:[0,0,0]
	s_setprio 0
	s_setprio 1
	v_mfma_scale_f32_16x16x128_f8f6f4 v[144:147], v[20:27], v[196:203], v[144:147], v219, v220 op_sel_hi:[0,0,0]
	v_mfma_scale_f32_16x16x128_f8f6f4 v[140:143], v[28:35], v[196:203], v[140:143], v219, v220 op_sel_hi:[0,0,0]
	v_mfma_scale_f32_16x16x128_f8f6f4 v[128:131], v[20:27], v[204:211], v[128:131], v219, v220 op_sel_hi:[0,0,0]
	v_mfma_scale_f32_16x16x128_f8f6f4 v[124:127], v[28:35], v[204:211], v[124:127], v219, v220 op_sel_hi:[0,0,0]
	v_mfma_scale_f32_16x16x128_f8f6f4 v[112:115], v[20:27], v[226:233], v[112:115], v219, v220 op_sel_hi:[0,0,0]
	v_mfma_scale_f32_16x16x128_f8f6f4 v[108:111], v[28:35], v[226:233], v[108:111], v219, v220 op_sel_hi:[0,0,0]
	v_mfma_scale_f32_16x16x128_f8f6f4 v[104:107], v[20:27], v[234:241], v[104:107], v219, v220 op_sel_hi:[0,0,0]
	v_mfma_scale_f32_16x16x128_f8f6f4 v[100:103], v[28:35], v[234:241], v[100:103], v219, v220 op_sel_hi:[0,0,0]
	s_setprio 0
	s_barrier
	s_add_i32 s42, s62, s10
	v_lshl_add_u64 v[174:175], v[182:183], 0, s[6:7]
	s_mov_b32 m0, s42
	ds_read_b128 v[196:199], v193 offset:49152
	ds_read_b128 v[204:207], v193 offset:51200
	ds_read_b128 v[200:203], v194 offset:49152
	ds_read_b128 v[208:211], v194 offset:51200
	ds_read_b128 v[226:229], v193 offset:53248
	ds_read_b128 v[234:237], v193 offset:55296
	ds_read_b128 v[230:233], v194 offset:53248
	ds_read_b128 v[238:241], v194 offset:55296
	global_load_lds_dwordx4 v[174:175], off
	s_add_i32 m0, s42, 0x2000
	s_add_u32 s42, s44, 0xb0080
	v_lshl_add_u64 v[174:175], v[184:185], 0, s[6:7]
	s_addc_u32 s43, s45, 0
	s_add_i32 s44, s63, s10
	global_load_lds_dwordx4 v[174:175], off
	v_lshl_add_u64 v[174:175], s[42:43], 0, v[2:3]
	s_mov_b32 m0, s44
	s_nop 0
	global_load_lds_dwordx4 v[174:175], off
	v_lshl_add_u64 v[174:175], s[42:43], 0, v[164:165]
	s_add_i32 m0, s44, 0x2000
	s_nop 0
	global_load_lds_dwordx4 v[174:175], off
	v_lshl_add_u64 v[174:175], v[186:187], 0, s[6:7]
	s_mov_b32 m0, s52
	s_nop 0
	global_load_lds_dwordx4 v[174:175], off
	v_lshl_add_u64 v[174:175], v[188:189], 0, s[6:7]
	s_mov_b32 m0, s53
	s_nop 0
	global_load_lds_dwordx4 v[174:175], off
	s_waitcnt vmcnt(8)
	s_waitcnt lgkmcnt(0)
	s_barrier
	s_setprio 1
	s_waitcnt lgkmcnt(0)
	v_mfma_scale_f32_16x16x128_f8f6f4 v[96:99], v[4:11], v[196:203], v[96:99], v219, v220 op_sel_hi:[0,0,0]
	v_mfma_scale_f32_16x16x128_f8f6f4 v[92:95], v[12:19], v[196:203], v[92:95], v219, v220 op_sel_hi:[0,0,0]
	v_mfma_scale_f32_16x16x128_f8f6f4 v[88:91], v[4:11], v[204:211], v[88:91], v219, v220 op_sel_hi:[0,0,0]
	v_mfma_scale_f32_16x16x128_f8f6f4 v[84:87], v[12:19], v[204:211], v[84:87], v219, v220 op_sel_hi:[0,0,0]
	v_mfma_scale_f32_16x16x128_f8f6f4 v[72:75], v[4:11], v[226:233], v[72:75], v219, v220 op_sel_hi:[0,0,0]
	v_mfma_scale_f32_16x16x128_f8f6f4 v[68:71], v[12:19], v[226:233], v[68:71], v219, v220 op_sel_hi:[0,0,0]
	v_mfma_scale_f32_16x16x128_f8f6f4 v[56:59], v[4:11], v[234:241], v[56:59], v219, v220 op_sel_hi:[0,0,0]
	v_mfma_scale_f32_16x16x128_f8f6f4 v[52:55], v[12:19], v[234:241], v[52:55], v219, v220 op_sel_hi:[0,0,0]
	s_setprio 0
	s_setprio 1
	v_mfma_scale_f32_16x16x128_f8f6f4 v[80:83], v[20:27], v[196:203], v[80:83], v219, v220 op_sel_hi:[0,0,0]
	v_mfma_scale_f32_16x16x128_f8f6f4 v[76:79], v[28:35], v[196:203], v[76:79], v219, v220 op_sel_hi:[0,0,0]
	v_mfma_scale_f32_16x16x128_f8f6f4 v[64:67], v[20:27], v[204:211], v[64:67], v219, v220 op_sel_hi:[0,0,0]
	v_mfma_scale_f32_16x16x128_f8f6f4 v[60:63], v[28:35], v[204:211], v[60:63], v219, v220 op_sel_hi:[0,0,0]
	v_mfma_scale_f32_16x16x128_f8f6f4 v[48:51], v[20:27], v[226:233], v[48:51], v219, v220 op_sel_hi:[0,0,0]
	v_mfma_scale_f32_16x16x128_f8f6f4 v[44:47], v[28:35], v[226:233], v[44:47], v219, v220 op_sel_hi:[0,0,0]
	v_mfma_scale_f32_16x16x128_f8f6f4 v[40:43], v[20:27], v[234:241], v[40:43], v219, v220 op_sel_hi:[0,0,0]
	v_mfma_scale_f32_16x16x128_f8f6f4 v[36:39], v[28:35], v[234:241], v[36:39], v219, v220 op_sel_hi:[0,0,0]
	s_setprio 0
	s_barrier
	s_add_i32 s61, s61, 2
	s_add_u32 s40, s40, 0x100
	s_addc_u32 s41, s41, 0
	s_add_u32 s59, s59, 0x100
	s_addc_u32 s60, s60, 0
	s_cmp_gt_u32 s61, 41
	s_cbranch_scc0 .LBB0_1894
	s_nop 15
	s_nop 15
	s_and_b64 vcc, exec, s[36:37]
	s_cbranch_vccz .LBB0_1897
	s_barrier

.LBB0_1938:
	v_lshrrev_b32_e32 v19, 4, v18
	v_and_b32_e32 v20, 15, v18
	s_lshl_b32 s1, s1, 5
	v_lshl_or_b32 v1, s4, 6, v20
	v_bfe_u32 v19, v19, 1, 1
	s_lshl_b32 s4, s4, 13
	s_and_b32 s1, s1, 0x60
	s_add_i32 m0, s59, 0x18000
	v_lshl_add_u64 v[10:11], v[10:11], 0, s[6:7]
	v_lshl_or_b32 v24, v19, 10, s4
	s_lshr_b32 s4, s1, 3
	s_waitcnt vmcnt(2)
	s_barrier
	global_load_lds_dwordx4 v[10:11], off
	v_lshl_add_u64 v[8:9], v[8:9], 0, s[6:7]
	s_add_i32 m0, s59, 0x1a000
	s_add_i32 s64, s59, 0x8000
	s_add_i32 s65, s59, 0xa000
	v_or_b32_e32 v19, s4, v19
	global_load_lds_dwordx4 v[8:9], off
	v_lshl_add_u64 v[4:5], v[4:5], 0, s[6:7]
	s_mov_b32 m0, s64
	s_add_u32 s4, s46, 0x58080
	global_load_lds_dwordx4 v[4:5], off
	v_lshl_add_u64 v[4:5], v[6:7], 0, s[6:7]
	s_mov_b32 m0, s65
	s_addc_u32 s5, s47, 0
	global_load_lds_dwordx4 v[4:5], off
	s_add_i32 m0, s59, 0x1c000
	v_lshl_add_u64 v[4:5], s[4:5], 0, v[2:3]
	global_load_lds_dwordx4 v[4:5], off
	v_lshl_add_u64 v[4:5], s[4:5], 0, v[164:165]
	s_add_i32 m0, s59, 0x1e000
	s_movk_i32 s4, 0xb00
	global_load_lds_dwordx4 v[4:5], off
	v_bfe_u32 v21, v18, 4, 2
	v_lshrrev_b32_e32 v5, 1, v16
	v_mul_lo_u32 v4, v15, s4
	s_mov_b32 s5, 0xb000
	s_cmpk_lt_u32 s0, 0x100
	v_lshl_or_b32 v192, v21, 3, s1
	v_mad_u64_u32 v[4:5], s[0:1], v5, s5, v[4:5]
	v_and_b32_e32 v5, 1, v16
	v_lshlrev_b32_e32 v22, 1, v18
	v_lshl_or_b32 v4, v5, 6, v4
	v_and_b32_e32 v22, 32, v22
	v_lshlrev_b32_e32 v20, 6, v20
	v_lshlrev_b32_e32 v18, 2, v18
	v_lshl_add_u32 v170, v17, 1, v4
	v_lshrrev_b32_e32 v5, 1, v12
	v_mul_lo_u32 v4, v13, s4
	v_or_b32_e32 v23, v20, v22
	v_and_b32_e32 v18, 32, v18
	v_mad_u64_u32 v[4:5], s[0:1], v5, s5, v[4:5]
	v_bitop3_b32 v20, v20, v18, v22 bitop3:0x36
	v_bitop3_b32 v25, v23, v18, 16 bitop3:0x36
	s_waitcnt vmcnt(6)
	v_and_b32_e32 v5, 1, v12
	v_or_b32_e32 v20, v20, v24
	v_or_b32_e32 v22, 16, v23
	v_or_b32_e32 v24, v25, v24
	v_lshlrev_b32_e32 v19, 10, v19
	v_lshl_or_b32 v4, v5, 6, v4
	v_bitop3_b32 v190, v19, v23, v18 bitop3:0xf6
	v_bitop3_b32 v191, v22, v19, v18 bitop3:0xde
	s_cselect_b64 s[38:39], -1, 0
	s_ashr_i32 s15, s14, 31
	v_mov_b32_e32 v171, v3
	v_lshl_add_u32 v172, v14, 1, v4
	v_mov_b32_e32 v173, v3
	s_mov_b32 s67, 0
	v_add_u32_e32 v193, 0, v20
	v_add_u32_e32 v194, 0, v24
	v_and_b32_e32 v193, 15, v0
	v_lshlrev_b32_e32 v193, 6, v193
	v_bfe_u32 v194, v0, 4, 2
	v_lshl_or_b32 v193, v194, 4, v193
	v_and_b32_e32 v194, 8, v0
	v_lshlrev_b32_e32 v194, 2, v194
	v_xor_b32_e32 v193, v193, v194
	v_bfe_u32 v190, v0, 6, 2
	v_lshl_or_b32 v190, v190, 12, v193
	v_or_b32_e32 v191, 0x400, v190
	v_add_u32_e32 v190, 0x10000, v190
	v_lshrrev_b32_e32 v194, 8, v0
	v_lshl_or_b32 v193, v194, 13, v193
	v_or_b32_e32 v194, 0x400, v193
	s_mov_b64 s[24:25], s[48:49]
	s_barrier
	s_branch .LBB0_1941

.LBB0_1948:
	s_add_u32 s43, s44, 0xfffa8080
	s_addc_u32 s46, s45, -1
	s_add_i32 s42, 0, 0x10000
	s_cmp_eq_u32 s72, 18
	s_cselect_b32 s49, s5, s46
	s_cselect_b32 s48, s4, s43
	s_cselect_b32 s47, s41, s71
	s_cselect_b32 s46, s40, s70
	s_add_i32 s43, 0, 0x14000
	ds_read_b128 v[20:23], v190
	ds_read_b128 v[28:31], v190 offset:2048
	ds_read_b128 v[24:27], v190 offset:1024
	ds_read_b128 v[32:35], v190 offset:3072
	ds_read_b128 v[4:7], v190 offset:16384
	ds_read_b128 v[12:15], v190 offset:18432
	ds_read_b128 v[8:11], v190 offset:17408
	ds_read_b128 v[16:19], v190 offset:19456
	v_lshl_add_u64 v[174:175], s[44:45], 0, v[170:171]
	s_add_i32 m0, s59, 0xc000
	ds_read_b128 v[178:181], v193
	ds_read_b128 v[196:199], v193 offset:2048
	ds_read_b128 v[182:185], v194
	ds_read_b128 v[200:203], v194 offset:2048
	ds_read_b128 v[204:207], v193 offset:4096
	ds_read_b128 v[226:229], v193 offset:6144
	ds_read_b128 v[208:211], v194 offset:4096
	ds_read_b128 v[230:233], v194 offset:6144
	global_load_lds_dwordx4 v[174:175], off
	v_lshl_add_u64 v[174:175], s[44:45], 0, v[172:173]
	s_add_i32 m0, s59, 0xe000
	s_nop 0
	global_load_lds_dwordx4 v[174:175], off
	s_waitcnt vmcnt(8)
	s_waitcnt lgkmcnt(0)
	s_barrier
	s_setprio 1
	s_waitcnt lgkmcnt(0)
	v_mfma_scale_f32_16x16x128_f8f6f4 v[160:163], v[20:27], v[178:185], v[160:163], v219, v220 op_sel_hi:[0,0,0]
	v_mfma_scale_f32_16x16x128_f8f6f4 v[156:159], v[28:35], v[178:185], v[156:159], v219, v220 op_sel_hi:[0,0,0]
	v_mfma_scale_f32_16x16x128_f8f6f4 v[152:155], v[20:27], v[196:203], v[152:155], v219, v220 op_sel_hi:[0,0,0]
	v_mfma_scale_f32_16x16x128_f8f6f4 v[148:151], v[28:35], v[196:203], v[148:151], v219, v220 op_sel_hi:[0,0,0]
	v_mfma_scale_f32_16x16x128_f8f6f4 v[136:139], v[20:27], v[204:211], v[136:139], v219, v220 op_sel_hi:[0,0,0]
	v_mfma_scale_f32_16x16x128_f8f6f4 v[132:135], v[28:35], v[204:211], v[132:135], v219, v220 op_sel_hi:[0,0,0]
	v_mfma_scale_f32_16x16x128_f8f6f4 v[120:123], v[20:27], v[226:233], v[120:123], v219, v220 op_sel_hi:[0,0,0]
	v_mfma_scale_f32_16x16x128_f8f6f4 v[116:119], v[28:35], v[226:233], v[116:119], v219, v220 op_sel_hi:[0,0,0]
	s_setprio 0
	s_setprio 1
	v_mfma_scale_f32_16x16x128_f8f6f4 v[144:147], v[4:11], v[178:185], v[144:147], v219, v220 op_sel_hi:[0,0,0]
	v_mfma_scale_f32_16x16x128_f8f6f4 v[140:143], v[12:19], v[178:185], v[140:143], v219, v220 op_sel_hi:[0,0,0]
	v_mfma_scale_f32_16x16x128_f8f6f4 v[128:131], v[4:11], v[196:203], v[128:131], v219, v220 op_sel_hi:[0,0,0]
	v_mfma_scale_f32_16x16x128_f8f6f4 v[124:127], v[12:19], v[196:203], v[124:127], v219, v220 op_sel_hi:[0,0,0]
	v_mfma_scale_f32_16x16x128_f8f6f4 v[112:115], v[4:11], v[204:211], v[112:115], v219, v220 op_sel_hi:[0,0,0]
	v_mfma_scale_f32_16x16x128_f8f6f4 v[108:111], v[12:19], v[204:211], v[108:111], v219, v220 op_sel_hi:[0,0,0]
	v_mfma_scale_f32_16x16x128_f8f6f4 v[104:107], v[4:11], v[226:233], v[104:107], v219, v220 op_sel_hi:[0,0,0]
	v_mfma_scale_f32_16x16x128_f8f6f4 v[100:103], v[12:19], v[226:233], v[100:103], v219, v220 op_sel_hi:[0,0,0]
	s_setprio 0
	s_barrier
	s_add_i32 s42, s42, s55
	v_lshl_add_u64 v[182:183], s[46:47], 0, v[2:3]
	s_mov_b32 m0, s42
	ds_read_b128 v[196:199], v193 offset:16384
	ds_read_b128 v[204:207], v193 offset:18432
	ds_read_b128 v[200:203], v194 offset:16384
	ds_read_b128 v[208:211], v194 offset:18432
	ds_read_b128 v[226:229], v193 offset:20480
	ds_read_b128 v[234:237], v193 offset:22528
	ds_read_b128 v[230:233], v194 offset:20480
	ds_read_b128 v[238:241], v194 offset:22528
	global_load_lds_dwordx4 v[182:183], off
	s_add_i32 m0, s42, 0x2000
	s_add_u32 s74, s46, 0x58000
	v_lshl_add_u64 v[184:185], s[46:47], 0, v[164:165]
	s_addc_u32 s75, s47, 0
	s_add_i32 s42, s43, s55
	global_load_lds_dwordx4 v[184:185], off
	v_lshl_add_u64 v[174:175], s[74:75], 0, v[2:3]
	s_mov_b32 m0, s42
	v_lshl_add_u64 v[186:187], s[48:49], 0, v[168:169]
	global_load_lds_dwordx4 v[174:175], off
	v_lshl_add_u64 v[174:175], s[74:75], 0, v[164:165]
	s_add_i32 m0, s42, 0x2000
	v_lshl_add_u64 v[188:189], s[48:49], 0, v[166:167]
	global_load_lds_dwordx4 v[174:175], off
	s_mov_b32 m0, s59
	s_nop 0
	global_load_lds_dwordx4 v[186:187], off
	s_mov_b32 m0, s60
	s_nop 0
	global_load_lds_dwordx4 v[188:189], off
	s_waitcnt vmcnt(8)
	s_waitcnt lgkmcnt(0)
	s_barrier
	s_setprio 1
	s_waitcnt lgkmcnt(0)
	v_mfma_scale_f32_16x16x128_f8f6f4 v[96:99], v[20:27], v[196:203], v[96:99], v219, v220 op_sel_hi:[0,0,0]
	v_mfma_scale_f32_16x16x128_f8f6f4 v[92:95], v[28:35], v[196:203], v[92:95], v219, v220 op_sel_hi:[0,0,0]
	v_mfma_scale_f32_16x16x128_f8f6f4 v[88:91], v[20:27], v[204:211], v[88:91], v219, v220 op_sel_hi:[0,0,0]
	v_mfma_scale_f32_16x16x128_f8f6f4 v[84:87], v[28:35], v[204:211], v[84:87], v219, v220 op_sel_hi:[0,0,0]
	v_mfma_scale_f32_16x16x128_f8f6f4 v[72:75], v[20:27], v[226:233], v[72:75], v219, v220 op_sel_hi:[0,0,0]
	v_mfma_scale_f32_16x16x128_f8f6f4 v[68:71], v[28:35], v[226:233], v[68:71], v219, v220 op_sel_hi:[0,0,0]
	v_mfma_scale_f32_16x16x128_f8f6f4 v[56:59], v[20:27], v[234:241], v[56:59], v219, v220 op_sel_hi:[0,0,0]
	v_mfma_scale_f32_16x16x128_f8f6f4 v[52:55], v[28:35], v[234:241], v[52:55], v219, v220 op_sel_hi:[0,0,0]
	s_setprio 0
	s_setprio 1
	v_mfma_scale_f32_16x16x128_f8f6f4 v[80:83], v[4:11], v[196:203], v[80:83], v219, v220 op_sel_hi:[0,0,0]
	v_mfma_scale_f32_16x16x128_f8f6f4 v[76:79], v[12:19], v[196:203], v[76:79], v219, v220 op_sel_hi:[0,0,0]
	v_mfma_scale_f32_16x16x128_f8f6f4 v[64:67], v[4:11], v[204:211], v[64:67], v219, v220 op_sel_hi:[0,0,0]
	v_mfma_scale_f32_16x16x128_f8f6f4 v[60:63], v[12:19], v[204:211], v[60:63], v219, v220 op_sel_hi:[0,0,0]
	v_mfma_scale_f32_16x16x128_f8f6f4 v[48:51], v[4:11], v[226:233], v[48:51], v219, v220 op_sel_hi:[0,0,0]
	v_mfma_scale_f32_16x16x128_f8f6f4 v[44:47], v[12:19], v[226:233], v[44:47], v219, v220 op_sel_hi:[0,0,0]
	v_mfma_scale_f32_16x16x128_f8f6f4 v[40:43], v[4:11], v[234:241], v[40:43], v219, v220 op_sel_hi:[0,0,0]
	v_mfma_scale_f32_16x16x128_f8f6f4 v[36:39], v[12:19], v[234:241], v[36:39], v219, v220 op_sel_hi:[0,0,0]
	s_setprio 0
	s_barrier
	s_add_i32 s73, 0, 0x18000
	s_add_i32 s74, 0, 0x1c000
	ds_read_b128 v[4:7], v190 offset:32768
	ds_read_b128 v[12:15], v190 offset:34816
	ds_read_b128 v[8:11], v190 offset:33792
	ds_read_b128 v[16:19], v190 offset:35840
	ds_read_b128 v[20:23], v190 offset:49152
	ds_read_b128 v[28:31], v190 offset:51200
	ds_read_b128 v[24:27], v190 offset:50176
	ds_read_b128 v[32:35], v190 offset:52224
	s_add_u32 s42, s48, 0x58000
	s_addc_u32 s43, s49, 0
	s_mov_b32 m0, s61
	v_lshl_add_u64 v[174:175], s[42:43], 0, v[168:169]
	ds_read_b128 v[196:199], v193 offset:32768
	ds_read_b128 v[204:207], v193 offset:34816
	ds_read_b128 v[200:203], v194 offset:32768
	ds_read_b128 v[208:211], v194 offset:34816
	ds_read_b128 v[226:229], v193 offset:36864
	ds_read_b128 v[234:237], v193 offset:38912
	ds_read_b128 v[230:233], v194 offset:36864
	ds_read_b128 v[238:241], v194 offset:38912
	global_load_lds_dwordx4 v[174:175], off
	v_lshl_add_u64 v[174:175], s[42:43], 0, v[166:167]
	s_mov_b32 m0, s62
	s_nop 0
	global_load_lds_dwordx4 v[174:175], off
	s_waitcnt vmcnt(8)
	s_waitcnt lgkmcnt(0)
	s_barrier
	s_setprio 1
	s_waitcnt lgkmcnt(0)
	v_mfma_scale_f32_16x16x128_f8f6f4 v[160:163], v[4:11], v[196:203], v[160:163], v219, v220 op_sel_hi:[0,0,0]
	v_mfma_scale_f32_16x16x128_f8f6f4 v[156:159], v[12:19], v[196:203], v[156:159], v219, v220 op_sel_hi:[0,0,0]
	v_mfma_scale_f32_16x16x128_f8f6f4 v[152:155], v[4:11], v[204:211], v[152:155], v219, v220 op_sel_hi:[0,0,0]
	v_mfma_scale_f32_16x16x128_f8f6f4 v[148:151], v[12:19], v[204:211], v[148:151], v219, v220 op_sel_hi:[0,0,0]
	v_mfma_scale_f32_16x16x128_f8f6f4 v[136:139], v[4:11], v[226:233], v[136:139], v219, v220 op_sel_hi:[0,0,0]
	v_mfma_scale_f32_16x16x128_f8f6f4 v[132:135], v[12:19], v[226:233], v[132:135], v219, v220 op_sel_hi:[0,0,0]
	v_mfma_scale_f32_16x16x128_f8f6f4 v[120:123], v[4:11], v[234:241], v[120:123], v219, v220 op_sel_hi:[0,0,0]
	v_mfma_scale_f32_16x16x128_f8f6f4 v[116:119], v[12:19], v[234:241], v[116:119], v219, v220 op_sel_hi:[0,0,0]
	s_setprio 0
	s_setprio 1
	v_mfma_scale_f32_16x16x128_f8f6f4 v[144:147], v[20:27], v[196:203], v[144:147], v219, v220 op_sel_hi:[0,0,0]
	v_mfma_scale_f32_16x16x128_f8f6f4 v[140:143], v[28:35], v[196:203], v[140:143], v219, v220 op_sel_hi:[0,0,0]
	v_mfma_scale_f32_16x16x128_f8f6f4 v[128:131], v[20:27], v[204:211], v[128:131], v219, v220 op_sel_hi:[0,0,0]
	v_mfma_scale_f32_16x16x128_f8f6f4 v[124:127], v[28:35], v[204:211], v[124:127], v219, v220 op_sel_hi:[0,0,0]
	v_mfma_scale_f32_16x16x128_f8f6f4 v[112:115], v[20:27], v[226:233], v[112:115], v219, v220 op_sel_hi:[0,0,0]
	v_mfma_scale_f32_16x16x128_f8f6f4 v[108:111], v[28:35], v[226:233], v[108:111], v219, v220 op_sel_hi:[0,0,0]
	v_mfma_scale_f32_16x16x128_f8f6f4 v[104:107], v[20:27], v[234:241], v[104:107], v219, v220 op_sel_hi:[0,0,0]
	v_mfma_scale_f32_16x16x128_f8f6f4 v[100:103], v[28:35], v[234:241], v[100:103], v219, v220 op_sel_hi:[0,0,0]
	s_setprio 0
	s_barrier
	s_add_i32 s42, s73, s55
	v_lshl_add_u64 v[174:175], v[182:183], 0, s[6:7]
	s_mov_b32 m0, s42
	ds_read_b128 v[196:199], v193 offset:49152
	ds_read_b128 v[204:207], v193 offset:51200
	ds_read_b128 v[200:203], v194 offset:49152
	ds_read_b128 v[208:211], v194 offset:51200
	ds_read_b128 v[226:229], v193 offset:53248
	ds_read_b128 v[234:237], v193 offset:55296
	ds_read_b128 v[230:233], v194 offset:53248
	ds_read_b128 v[238:241], v194 offset:55296
	global_load_lds_dwordx4 v[174:175], off
	s_add_i32 m0, s42, 0x2000
	s_add_u32 s42, s46, 0x58080
	v_lshl_add_u64 v[174:175], v[184:185], 0, s[6:7]
	s_addc_u32 s43, s47, 0
	s_add_i32 s46, s74, s55
	global_load_lds_dwordx4 v[174:175], off
	v_lshl_add_u64 v[174:175], s[42:43], 0, v[2:3]
	s_mov_b32 m0, s46
	s_nop 0
	global_load_lds_dwordx4 v[174:175], off
	v_lshl_add_u64 v[174:175], s[42:43], 0, v[164:165]
	s_add_i32 m0, s46, 0x2000
	s_nop 0
	global_load_lds_dwordx4 v[174:175], off
	v_lshl_add_u64 v[174:175], v[186:187], 0, s[6:7]
	s_mov_b32 m0, s64
	s_nop 0
	global_load_lds_dwordx4 v[174:175], off
	v_lshl_add_u64 v[174:175], v[188:189], 0, s[6:7]
	s_mov_b32 m0, s65
	s_nop 0
	global_load_lds_dwordx4 v[174:175], off
	s_waitcnt vmcnt(8)
	s_waitcnt lgkmcnt(0)
	s_barrier
	s_setprio 1
	s_waitcnt lgkmcnt(0)
	v_mfma_scale_f32_16x16x128_f8f6f4 v[96:99], v[4:11], v[196:203], v[96:99], v219, v220 op_sel_hi:[0,0,0]
	v_mfma_scale_f32_16x16x128_f8f6f4 v[92:95], v[12:19], v[196:203], v[92:95], v219, v220 op_sel_hi:[0,0,0]
	v_mfma_scale_f32_16x16x128_f8f6f4 v[88:91], v[4:11], v[204:211], v[88:91], v219, v220 op_sel_hi:[0,0,0]
	v_mfma_scale_f32_16x16x128_f8f6f4 v[84:87], v[12:19], v[204:211], v[84:87], v219, v220 op_sel_hi:[0,0,0]
	v_mfma_scale_f32_16x16x128_f8f6f4 v[72:75], v[4:11], v[226:233], v[72:75], v219, v220 op_sel_hi:[0,0,0]
	v_mfma_scale_f32_16x16x128_f8f6f4 v[68:71], v[12:19], v[226:233], v[68:71], v219, v220 op_sel_hi:[0,0,0]
	v_mfma_scale_f32_16x16x128_f8f6f4 v[56:59], v[4:11], v[234:241], v[56:59], v219, v220 op_sel_hi:[0,0,0]
	v_mfma_scale_f32_16x16x128_f8f6f4 v[52:55], v[12:19], v[234:241], v[52:55], v219, v220 op_sel_hi:[0,0,0]
	s_setprio 0
	s_setprio 1
	v_mfma_scale_f32_16x16x128_f8f6f4 v[80:83], v[20:27], v[196:203], v[80:83], v219, v220 op_sel_hi:[0,0,0]
	v_mfma_scale_f32_16x16x128_f8f6f4 v[76:79], v[28:35], v[196:203], v[76:79], v219, v220 op_sel_hi:[0,0,0]
	v_mfma_scale_f32_16x16x128_f8f6f4 v[64:67], v[20:27], v[204:211], v[64:67], v219, v220 op_sel_hi:[0,0,0]
	v_mfma_scale_f32_16x16x128_f8f6f4 v[60:63], v[28:35], v[204:211], v[60:63], v219, v220 op_sel_hi:[0,0,0]
	v_mfma_scale_f32_16x16x128_f8f6f4 v[48:51], v[20:27], v[226:233], v[48:51], v219, v220 op_sel_hi:[0,0,0]
	v_mfma_scale_f32_16x16x128_f8f6f4 v[44:47], v[28:35], v[226:233], v[44:47], v219, v220 op_sel_hi:[0,0,0]
	v_mfma_scale_f32_16x16x128_f8f6f4 v[40:43], v[20:27], v[234:241], v[40:43], v219, v220 op_sel_hi:[0,0,0]
	v_mfma_scale_f32_16x16x128_f8f6f4 v[36:39], v[28:35], v[234:241], v[36:39], v219, v220 op_sel_hi:[0,0,0]
	s_setprio 0
	s_barrier
	s_add_i32 s72, s72, 2
	s_add_u32 s44, s44, 0x100
	s_addc_u32 s45, s45, 0
	s_add_u32 s70, s70, 0x100
	s_addc_u32 s71, s71, 0
	s_cmp_gt_u32 s72, 19
	s_cbranch_scc0 .LBB0_1948
	s_nop 15
	s_nop 15
	s_and_b64 vcc, exec, s[38:39]
	s_cbranch_vccz .LBB0_1951
	s_barrier
